# GEMM K-loops: one more priority yield point (s_setprio 0 / s_setprio 1) in the middle of every MFMA group, so the loading partner wave gets issue windows twice as often (on top of v34)
# speedup vs baseline: 1.0115x; 1.0115x over previous
.LBB0_290:
	s_add_u32 s46, s44, 0xfffc0080
	s_addc_u32 s47, s45, -1
	s_add_i32 s62, 0, 0x10000
	s_cmp_eq_u32 s61, 12
	s_cselect_b32 s49, s1, s47
	s_cselect_b32 s48, s5, s46
	s_cselect_b32 s47, s35, s60
	s_cselect_b32 s46, s37, s59
	s_add_i32 s64, 0, 0x14000
	v_add_u32_e32 v158, s62, v148
	v_add_u32_e32 v174, s64, v148
	ds_read_b128 v[144:147], v158
	ds_read_b128 v[150:153], v158 offset:1024
	ds_read_b128 v[154:157], v158 offset:2048
	ds_read_b128 v[158:161], v158 offset:3072
	ds_read_b128 v[162:165], v174
	ds_read_b128 v[166:169], v174 offset:1024
	ds_read_b128 v[170:173], v174 offset:2048
	ds_read_b128 v[174:177], v174 offset:3072
	v_lshl_add_u64 v[210:211], s[44:45], 0, v[140:141]
	s_add_i32 m0, s50, 0xc000
	ds_read_b128 v[178:181], v149
	ds_read_b128 v[182:185], v149 offset:1024
	ds_read_b128 v[186:189], v149 offset:2048
	ds_read_b128 v[190:193], v149 offset:3072
	ds_read_b128 v[194:197], v149 offset:4096
	ds_read_b128 v[198:201], v149 offset:5120
	ds_read_b128 v[202:205], v149 offset:6144
	ds_read_b128 v[206:209], v149 offset:7168
	global_load_lds_dwordx4 v[210:211], off
	v_lshl_add_u64 v[210:211], s[44:45], 0, v[142:143]
	s_add_i32 m0, s50, 0xe000
	s_nop 0
	global_load_lds_dwordx4 v[210:211], off
	s_waitcnt vmcnt(8)
	s_waitcnt lgkmcnt(0)
	s_barrier
	s_setprio 1
	s_waitcnt lgkmcnt(0)
	v_mfma_f32_16x16x32_bf16 v[130:133], v[144:147], v[178:181], v[130:133]
	v_mfma_f32_16x16x32_bf16 v[126:129], v[154:157], v[178:181], v[126:129]
	v_mfma_f32_16x16x32_bf16 v[114:117], v[144:147], v[186:189], v[114:117]
	v_mfma_f32_16x16x32_bf16 v[110:113], v[154:157], v[186:189], v[110:113]
	v_mfma_f32_16x16x32_bf16 v[98:101], v[144:147], v[194:197], v[98:101]
	v_mfma_f32_16x16x32_bf16 v[94:97], v[154:157], v[194:197], v[94:97]
	v_mfma_f32_16x16x32_bf16 v[82:85], v[144:147], v[202:205], v[82:85]
	v_mfma_f32_16x16x32_bf16 v[78:81], v[154:157], v[202:205], v[78:81]
	s_setprio 0
	s_setprio 1
	v_mfma_f32_16x16x32_bf16 v[130:133], v[150:153], v[182:185], v[130:133]
	v_mfma_f32_16x16x32_bf16 v[126:129], v[158:161], v[182:185], v[126:129]
	v_mfma_f32_16x16x32_bf16 v[114:117], v[150:153], v[190:193], v[114:117]
	v_mfma_f32_16x16x32_bf16 v[110:113], v[158:161], v[190:193], v[110:113]
	v_mfma_f32_16x16x32_bf16 v[98:101], v[150:153], v[198:201], v[98:101]
	v_mfma_f32_16x16x32_bf16 v[94:97], v[158:161], v[198:201], v[94:97]
	v_mfma_f32_16x16x32_bf16 v[82:85], v[150:153], v[206:209], v[82:85]
	v_mfma_f32_16x16x32_bf16 v[78:81], v[158:161], v[206:209], v[78:81]
	s_setprio 0
	s_setprio 1
	v_mfma_f32_16x16x32_bf16 v[122:125], v[162:165], v[178:181], v[122:125]
	v_mfma_f32_16x16x32_bf16 v[118:121], v[170:173], v[178:181], v[118:121]
	v_mfma_f32_16x16x32_bf16 v[106:109], v[162:165], v[186:189], v[106:109]
	v_mfma_f32_16x16x32_bf16 v[102:105], v[170:173], v[186:189], v[102:105]
	v_mfma_f32_16x16x32_bf16 v[90:93], v[162:165], v[194:197], v[90:93]
	v_mfma_f32_16x16x32_bf16 v[86:89], v[170:173], v[194:197], v[86:89]
	v_mfma_f32_16x16x32_bf16 v[74:77], v[162:165], v[202:205], v[74:77]
	v_mfma_f32_16x16x32_bf16 v[70:73], v[170:173], v[202:205], v[70:73]
	s_setprio 0
	s_setprio 1
	v_mfma_f32_16x16x32_bf16 v[122:125], v[166:169], v[182:185], v[122:125]
	v_mfma_f32_16x16x32_bf16 v[118:121], v[174:177], v[182:185], v[118:121]
	v_mfma_f32_16x16x32_bf16 v[106:109], v[166:169], v[190:193], v[106:109]
	v_mfma_f32_16x16x32_bf16 v[102:105], v[174:177], v[190:193], v[102:105]
	v_mfma_f32_16x16x32_bf16 v[90:93], v[166:169], v[198:201], v[90:93]
	v_mfma_f32_16x16x32_bf16 v[86:89], v[174:177], v[198:201], v[86:89]
	v_mfma_f32_16x16x32_bf16 v[74:77], v[166:169], v[206:209], v[74:77]
	v_mfma_f32_16x16x32_bf16 v[70:73], v[174:177], v[206:209], v[70:73]
	s_setprio 0
	s_barrier
	s_add_i32 s62, s62, s27
	v_lshl_add_u64 v[210:211], s[46:47], 0, v[0:1]
	s_mov_b32 m0, s62
	ds_read_b128 v[178:181], v149 offset:16384
	ds_read_b128 v[182:185], v149 offset:17408
	ds_read_b128 v[186:189], v149 offset:18432
	ds_read_b128 v[190:193], v149 offset:19456
	ds_read_b128 v[194:197], v149 offset:20480
	ds_read_b128 v[198:201], v149 offset:21504
	ds_read_b128 v[202:205], v149 offset:22528
	ds_read_b128 v[206:209], v149 offset:23552
	global_load_lds_dwordx4 v[210:211], off
	s_add_i32 m0, s62, 0x2000
	s_add_u32 s62, s46, 0x40000
	v_lshl_add_u64 v[212:213], s[46:47], 0, v[138:139]
	s_addc_u32 s63, s47, 0
	s_add_i32 s64, s64, s27
	global_load_lds_dwordx4 v[212:213], off
	v_lshl_add_u64 v[216:217], s[62:63], 0, v[0:1]
	s_mov_b32 m0, s64
	v_lshl_add_u64 v[218:219], s[48:49], 0, v[136:137]
	global_load_lds_dwordx4 v[216:217], off
	v_lshl_add_u64 v[216:217], s[62:63], 0, v[138:139]
	s_add_i32 m0, s64, 0x2000
	s_nop 0
	global_load_lds_dwordx4 v[216:217], off
	v_lshl_add_u64 v[216:217], s[48:49], 0, v[134:135]
	s_mov_b32 m0, s50
	s_nop 0
	global_load_lds_dwordx4 v[216:217], off
	s_mov_b32 m0, s51
	s_nop 0
	global_load_lds_dwordx4 v[218:219], off
	s_waitcnt vmcnt(8)
	s_waitcnt lgkmcnt(0)
	s_barrier
	s_setprio 1
	s_waitcnt lgkmcnt(0)
	v_mfma_f32_16x16x32_bf16 v[66:69], v[144:147], v[178:181], v[66:69]
	v_mfma_f32_16x16x32_bf16 v[62:65], v[154:157], v[178:181], v[62:65]
	v_mfma_f32_16x16x32_bf16 v[50:53], v[144:147], v[186:189], v[50:53]
	v_mfma_f32_16x16x32_bf16 v[46:49], v[154:157], v[186:189], v[46:49]
	v_mfma_f32_16x16x32_bf16 v[34:37], v[144:147], v[194:197], v[34:37]
	v_mfma_f32_16x16x32_bf16 v[30:33], v[154:157], v[194:197], v[30:33]
	v_mfma_f32_16x16x32_bf16 v[18:21], v[144:147], v[202:205], v[18:21]
	v_mfma_f32_16x16x32_bf16 v[14:17], v[154:157], v[202:205], v[14:17]
	s_setprio 0
	s_setprio 1
	v_mfma_f32_16x16x32_bf16 v[66:69], v[150:153], v[182:185], v[66:69]
	v_mfma_f32_16x16x32_bf16 v[62:65], v[158:161], v[182:185], v[62:65]
	v_mfma_f32_16x16x32_bf16 v[50:53], v[150:153], v[190:193], v[50:53]
	v_mfma_f32_16x16x32_bf16 v[46:49], v[158:161], v[190:193], v[46:49]
	v_mfma_f32_16x16x32_bf16 v[34:37], v[150:153], v[198:201], v[34:37]
	v_mfma_f32_16x16x32_bf16 v[30:33], v[158:161], v[198:201], v[30:33]
	v_mfma_f32_16x16x32_bf16 v[18:21], v[150:153], v[206:209], v[18:21]
	v_mfma_f32_16x16x32_bf16 v[14:17], v[158:161], v[206:209], v[14:17]
	s_setprio 0
	s_setprio 1
	v_mfma_f32_16x16x32_bf16 v[58:61], v[162:165], v[178:181], v[58:61]
	v_mfma_f32_16x16x32_bf16 v[54:57], v[170:173], v[178:181], v[54:57]
	v_mfma_f32_16x16x32_bf16 v[42:45], v[162:165], v[186:189], v[42:45]
	v_mfma_f32_16x16x32_bf16 v[38:41], v[170:173], v[186:189], v[38:41]
	v_mfma_f32_16x16x32_bf16 v[26:29], v[162:165], v[194:197], v[26:29]
	v_mfma_f32_16x16x32_bf16 v[22:25], v[170:173], v[194:197], v[22:25]
	v_mfma_f32_16x16x32_bf16 v[10:13], v[162:165], v[202:205], v[10:13]
	v_mfma_f32_16x16x32_bf16 v[6:9], v[170:173], v[202:205], v[6:9]
	s_setprio 0
	s_setprio 1
	v_mfma_f32_16x16x32_bf16 v[58:61], v[166:169], v[182:185], v[58:61]
	v_mfma_f32_16x16x32_bf16 v[54:57], v[174:177], v[182:185], v[54:57]
	v_mfma_f32_16x16x32_bf16 v[42:45], v[166:169], v[190:193], v[42:45]
	v_mfma_f32_16x16x32_bf16 v[38:41], v[174:177], v[190:193], v[38:41]
	v_mfma_f32_16x16x32_bf16 v[26:29], v[166:169], v[198:201], v[26:29]
	v_mfma_f32_16x16x32_bf16 v[22:25], v[174:177], v[198:201], v[22:25]
	v_mfma_f32_16x16x32_bf16 v[10:13], v[166:169], v[206:209], v[10:13]
	v_mfma_f32_16x16x32_bf16 v[6:9], v[174:177], v[206:209], v[6:9]
	s_setprio 0
	s_barrier
	s_add_i32 s62, 0, 0x18000
	s_add_i32 s63, 0, 0x1c000
	v_add_u32_e32 v158, s62, v148
	v_add_u32_e32 v174, s63, v148
	ds_read_b128 v[144:147], v158
	ds_read_b128 v[150:153], v158 offset:1024
	ds_read_b128 v[154:157], v158 offset:2048
	ds_read_b128 v[158:161], v158 offset:3072
	ds_read_b128 v[162:165], v174
	ds_read_b128 v[166:169], v174 offset:1024
	ds_read_b128 v[170:173], v174 offset:2048
	ds_read_b128 v[174:177], v174 offset:3072
	s_add_u32 s48, s48, 0x40000
	s_addc_u32 s49, s49, 0
	s_mov_b32 m0, s52
	v_lshl_add_u64 v[220:221], s[48:49], 0, v[134:135]
	ds_read_b128 v[178:181], v149 offset:32768
	ds_read_b128 v[182:185], v149 offset:33792
	ds_read_b128 v[186:189], v149 offset:34816
	ds_read_b128 v[190:193], v149 offset:35840
	ds_read_b128 v[194:197], v149 offset:36864
	ds_read_b128 v[198:201], v149 offset:37888
	ds_read_b128 v[202:205], v149 offset:38912
	ds_read_b128 v[206:209], v149 offset:39936
	global_load_lds_dwordx4 v[220:221], off
	v_lshl_add_u64 v[220:221], s[48:49], 0, v[136:137]
	s_mov_b32 m0, s53
	s_nop 0
	global_load_lds_dwordx4 v[220:221], off
	s_waitcnt vmcnt(8)
	s_waitcnt lgkmcnt(0)
	s_barrier
	s_setprio 1
	s_waitcnt lgkmcnt(0)
	v_mfma_f32_16x16x32_bf16 v[130:133], v[144:147], v[178:181], v[130:133]
	v_mfma_f32_16x16x32_bf16 v[126:129], v[154:157], v[178:181], v[126:129]
	v_mfma_f32_16x16x32_bf16 v[114:117], v[144:147], v[186:189], v[114:117]
	v_mfma_f32_16x16x32_bf16 v[110:113], v[154:157], v[186:189], v[110:113]
	v_mfma_f32_16x16x32_bf16 v[98:101], v[144:147], v[194:197], v[98:101]
	v_mfma_f32_16x16x32_bf16 v[94:97], v[154:157], v[194:197], v[94:97]
	v_mfma_f32_16x16x32_bf16 v[82:85], v[144:147], v[202:205], v[82:85]
	v_mfma_f32_16x16x32_bf16 v[78:81], v[154:157], v[202:205], v[78:81]
	s_setprio 0
	s_setprio 1
	v_mfma_f32_16x16x32_bf16 v[130:133], v[150:153], v[182:185], v[130:133]
	v_mfma_f32_16x16x32_bf16 v[126:129], v[158:161], v[182:185], v[126:129]
	v_mfma_f32_16x16x32_bf16 v[114:117], v[150:153], v[190:193], v[114:117]
	v_mfma_f32_16x16x32_bf16 v[110:113], v[158:161], v[190:193], v[110:113]
	v_mfma_f32_16x16x32_bf16 v[98:101], v[150:153], v[198:201], v[98:101]
	v_mfma_f32_16x16x32_bf16 v[94:97], v[158:161], v[198:201], v[94:97]
	v_mfma_f32_16x16x32_bf16 v[82:85], v[150:153], v[206:209], v[82:85]
	v_mfma_f32_16x16x32_bf16 v[78:81], v[158:161], v[206:209], v[78:81]
	s_setprio 0
	s_setprio 1
	v_mfma_f32_16x16x32_bf16 v[122:125], v[162:165], v[178:181], v[122:125]
	v_mfma_f32_16x16x32_bf16 v[118:121], v[170:173], v[178:181], v[118:121]
	v_mfma_f32_16x16x32_bf16 v[106:109], v[162:165], v[186:189], v[106:109]
	v_mfma_f32_16x16x32_bf16 v[102:105], v[170:173], v[186:189], v[102:105]
	v_mfma_f32_16x16x32_bf16 v[90:93], v[162:165], v[194:197], v[90:93]
	v_mfma_f32_16x16x32_bf16 v[86:89], v[170:173], v[194:197], v[86:89]
	v_mfma_f32_16x16x32_bf16 v[74:77], v[162:165], v[202:205], v[74:77]
	v_mfma_f32_16x16x32_bf16 v[70:73], v[170:173], v[202:205], v[70:73]
	s_setprio 0
	s_setprio 1
	v_mfma_f32_16x16x32_bf16 v[122:125], v[166:169], v[182:185], v[122:125]
	v_mfma_f32_16x16x32_bf16 v[118:121], v[174:177], v[182:185], v[118:121]
	v_mfma_f32_16x16x32_bf16 v[106:109], v[166:169], v[190:193], v[106:109]
	v_mfma_f32_16x16x32_bf16 v[102:105], v[174:177], v[190:193], v[102:105]
	v_mfma_f32_16x16x32_bf16 v[90:93], v[166:169], v[198:201], v[90:93]
	v_mfma_f32_16x16x32_bf16 v[86:89], v[174:177], v[198:201], v[86:89]
	v_mfma_f32_16x16x32_bf16 v[74:77], v[166:169], v[206:209], v[74:77]
	v_mfma_f32_16x16x32_bf16 v[70:73], v[174:177], v[206:209], v[70:73]
	s_setprio 0
	s_barrier
	s_add_i32 s48, s62, s27
	v_lshl_add_u64 v[210:211], v[210:211], 0, s[66:67]
	s_mov_b32 m0, s48
	ds_read_b128 v[178:181], v149 offset:49152
	ds_read_b128 v[182:185], v149 offset:50176
	ds_read_b128 v[186:189], v149 offset:51200
	ds_read_b128 v[190:193], v149 offset:52224
	ds_read_b128 v[194:197], v149 offset:53248
	ds_read_b128 v[198:201], v149 offset:54272
	ds_read_b128 v[202:205], v149 offset:55296
	ds_read_b128 v[206:209], v149 offset:56320
	global_load_lds_dwordx4 v[210:211], off
	s_add_i32 m0, s48, 0x2000
	s_add_u32 s46, s46, 0x40080
	v_lshl_add_u64 v[210:211], v[212:213], 0, s[66:67]
	s_addc_u32 s47, s47, 0
	s_add_i32 s48, s63, s27
	global_load_lds_dwordx4 v[210:211], off
	v_lshl_add_u64 v[210:211], s[46:47], 0, v[0:1]
	s_mov_b32 m0, s48
	s_nop 0
	global_load_lds_dwordx4 v[210:211], off
	v_lshl_add_u64 v[210:211], s[46:47], 0, v[138:139]
	s_add_i32 m0, s48, 0x2000
	s_nop 0
	global_load_lds_dwordx4 v[210:211], off
	v_lshl_add_u64 v[210:211], v[216:217], 0, s[66:67]
	s_mov_b32 m0, s56
	s_nop 0
	global_load_lds_dwordx4 v[210:211], off
	v_lshl_add_u64 v[210:211], v[218:219], 0, s[66:67]
	s_mov_b32 m0, s57
	s_nop 0
	global_load_lds_dwordx4 v[210:211], off
	s_waitcnt vmcnt(8)
	s_waitcnt lgkmcnt(0)
	s_barrier
	s_setprio 1
	s_waitcnt lgkmcnt(0)
	v_mfma_f32_16x16x32_bf16 v[66:69], v[144:147], v[178:181], v[66:69]
	v_mfma_f32_16x16x32_bf16 v[62:65], v[154:157], v[178:181], v[62:65]
	v_mfma_f32_16x16x32_bf16 v[50:53], v[144:147], v[186:189], v[50:53]
	v_mfma_f32_16x16x32_bf16 v[46:49], v[154:157], v[186:189], v[46:49]
	v_mfma_f32_16x16x32_bf16 v[34:37], v[144:147], v[194:197], v[34:37]
	v_mfma_f32_16x16x32_bf16 v[30:33], v[154:157], v[194:197], v[30:33]
	v_mfma_f32_16x16x32_bf16 v[18:21], v[144:147], v[202:205], v[18:21]
	v_mfma_f32_16x16x32_bf16 v[14:17], v[154:157], v[202:205], v[14:17]
	s_setprio 0
	s_setprio 1
	v_mfma_f32_16x16x32_bf16 v[66:69], v[150:153], v[182:185], v[66:69]
	v_mfma_f32_16x16x32_bf16 v[62:65], v[158:161], v[182:185], v[62:65]
	v_mfma_f32_16x16x32_bf16 v[50:53], v[150:153], v[190:193], v[50:53]
	v_mfma_f32_16x16x32_bf16 v[46:49], v[158:161], v[190:193], v[46:49]
	v_mfma_f32_16x16x32_bf16 v[34:37], v[150:153], v[198:201], v[34:37]
	v_mfma_f32_16x16x32_bf16 v[30:33], v[158:161], v[198:201], v[30:33]
	v_mfma_f32_16x16x32_bf16 v[18:21], v[150:153], v[206:209], v[18:21]
	v_mfma_f32_16x16x32_bf16 v[14:17], v[158:161], v[206:209], v[14:17]
	s_setprio 0
	s_setprio 1
	v_mfma_f32_16x16x32_bf16 v[58:61], v[162:165], v[178:181], v[58:61]
	v_mfma_f32_16x16x32_bf16 v[54:57], v[170:173], v[178:181], v[54:57]
	v_mfma_f32_16x16x32_bf16 v[42:45], v[162:165], v[186:189], v[42:45]
	v_mfma_f32_16x16x32_bf16 v[38:41], v[170:173], v[186:189], v[38:41]
	v_mfma_f32_16x16x32_bf16 v[26:29], v[162:165], v[194:197], v[26:29]
	v_mfma_f32_16x16x32_bf16 v[22:25], v[170:173], v[194:197], v[22:25]
	v_mfma_f32_16x16x32_bf16 v[10:13], v[162:165], v[202:205], v[10:13]
	v_mfma_f32_16x16x32_bf16 v[6:9], v[170:173], v[202:205], v[6:9]
	s_setprio 0
	s_setprio 1
	v_mfma_f32_16x16x32_bf16 v[58:61], v[166:169], v[182:185], v[58:61]
	v_mfma_f32_16x16x32_bf16 v[54:57], v[174:177], v[182:185], v[54:57]
	v_mfma_f32_16x16x32_bf16 v[42:45], v[166:169], v[190:193], v[42:45]
	v_mfma_f32_16x16x32_bf16 v[38:41], v[174:177], v[190:193], v[38:41]
	v_mfma_f32_16x16x32_bf16 v[26:29], v[166:169], v[198:201], v[26:29]
	v_mfma_f32_16x16x32_bf16 v[22:25], v[174:177], v[198:201], v[22:25]
	v_mfma_f32_16x16x32_bf16 v[10:13], v[166:169], v[206:209], v[10:13]
	v_mfma_f32_16x16x32_bf16 v[6:9], v[174:177], v[206:209], v[6:9]
	s_setprio 0
	s_barrier
	s_add_i32 s61, s61, 2
	s_add_u32 s44, s44, 0x100
	s_addc_u32 s45, s45, 0
	s_add_u32 s59, s59, 0x100
	s_addc_u32 s60, s60, 0
	s_cmp_gt_u32 s61, 13
	s_cbranch_scc0 .LBB0_290
	s_and_b64 vcc, exec, s[30:31]
	s_cbranch_vccz .LBB0_293
	s_barrier

.Lrw_done_ip8_0:
	s_waitcnt lgkmcnt(0)
	s_barrier
	s_setprio 1
	s_waitcnt lgkmcnt(0)
	v_mfma_scale_f32_16x16x128_f8f6f4 v[158:161], v[18:25], v[172:179], 0, v234, v235 op_sel_hi:[0,0,0]
	v_mfma_scale_f32_16x16x128_f8f6f4 v[154:157], v[26:33], v[172:179], 0, v234, v235 op_sel_hi:[0,0,0]
	v_mfma_scale_f32_16x16x128_f8f6f4 v[150:153], v[18:25], v[198:205], 0, v234, v235 op_sel_hi:[0,0,0]
	v_mfma_scale_f32_16x16x128_f8f6f4 v[146:149], v[26:33], v[198:205], 0, v234, v235 op_sel_hi:[0,0,0]
	s_setprio 0
	s_setprio 1
	v_mfma_scale_f32_16x16x128_f8f6f4 v[142:145], v[18:25], v[206:213], 0, v234, v235 op_sel_hi:[0,0,0]
	v_mfma_scale_f32_16x16x128_f8f6f4 v[138:141], v[26:33], v[206:213], 0, v234, v235 op_sel_hi:[0,0,0]
	v_mfma_scale_f32_16x16x128_f8f6f4 v[134:137], v[18:25], v[216:223], 0, v234, v235 op_sel_hi:[0,0,0]
	v_mfma_scale_f32_16x16x128_f8f6f4 v[130:133], v[26:33], v[216:223], 0, v234, v235 op_sel_hi:[0,0,0]
	s_setprio 0
	s_setprio 1
	v_mfma_scale_f32_16x16x128_f8f6f4 v[126:129], v[2:9], v[172:179], 0, v234, v235 op_sel_hi:[0,0,0]
	v_mfma_scale_f32_16x16x128_f8f6f4 v[122:125], v[10:17], v[172:179], 0, v234, v235 op_sel_hi:[0,0,0]
	v_mfma_scale_f32_16x16x128_f8f6f4 v[118:121], v[2:9], v[198:205], 0, v234, v235 op_sel_hi:[0,0,0]
	v_mfma_scale_f32_16x16x128_f8f6f4 v[114:117], v[10:17], v[198:205], 0, v234, v235 op_sel_hi:[0,0,0]
	s_setprio 0
	s_setprio 1
	v_mfma_scale_f32_16x16x128_f8f6f4 v[110:113], v[2:9], v[206:213], 0, v234, v235 op_sel_hi:[0,0,0]
	v_mfma_scale_f32_16x16x128_f8f6f4 v[106:109], v[10:17], v[206:213], 0, v234, v235 op_sel_hi:[0,0,0]
	v_mfma_scale_f32_16x16x128_f8f6f4 v[102:105], v[2:9], v[216:223], 0, v234, v235 op_sel_hi:[0,0,0]
	v_mfma_scale_f32_16x16x128_f8f6f4 v[98:101], v[10:17], v[216:223], 0, v234, v235 op_sel_hi:[0,0,0]
	s_setprio 0
	s_barrier
	v_lshl_add_u64 v[172:173], s[44:45], 0, v[0:1]
	s_mov_b64 s[74:75], 0x100
	s_mov_b32 m0, s58
	v_lshl_add_u64 v[174:175], v[172:173], 0, s[74:75]
	ds_read_b128 v[198:201], v196 offset:16384
	ds_read_b128 v[202:205], v196 offset:17408
	ds_read_b128 v[206:209], v196 offset:18432
	ds_read_b128 v[210:213], v196 offset:19456
	ds_read_b128 v[216:219], v196 offset:20480
	ds_read_b128 v[220:223], v196 offset:21504
	ds_read_b128 v[224:227], v196 offset:22528
	ds_read_b128 v[228:231], v196 offset:23552
	global_load_lds_dwordx4 v[174:175], off
	v_lshl_add_u64 v[174:175], s[44:45], 0, v[166:167]
	s_add_u32 s48, s44, 0x20100
	v_lshl_add_u64 v[176:177], v[174:175], 0, s[74:75]
	s_mov_b32 m0, s59
	s_addc_u32 s49, s45, 0
	global_load_lds_dwordx4 v[176:177], off
	v_lshl_add_u64 v[176:177], s[48:49], 0, v[0:1]
	s_mov_b32 m0, s60
	s_nop 0
	global_load_lds_dwordx4 v[176:177], off
	v_lshl_add_u64 v[176:177], s[48:49], 0, v[166:167]
	s_mov_b32 m0, s61
	s_nop 0
	global_load_lds_dwordx4 v[176:177], off
	v_lshl_add_u64 v[176:177], s[46:47], 0, v[162:163]
	v_lshl_add_u64 v[178:179], v[176:177], 0, s[74:75]
	s_mov_b32 m0, s57
	s_nop 0
	global_load_lds_dwordx4 v[178:179], off
	v_lshl_add_u64 v[178:179], s[46:47], 0, v[164:165]
	v_lshl_add_u64 v[232:233], v[178:179], 0, s[74:75]
	s_mov_b32 m0, s62
	s_nop 0
	global_load_lds_dwordx4 v[232:233], off
	s_cmp_eq_u32 s50, 1
	s_cbranch_scc1 .Lrw_first_ip8_1
	s_waitcnt vmcnt(24)
	s_branch .Lrw_done_ip8_1

.Lrw_done_ip8_1:
	s_waitcnt lgkmcnt(0)
	s_barrier
	s_setprio 1
	s_waitcnt lgkmcnt(0)
	v_mfma_scale_f32_16x16x128_f8f6f4 v[94:97], v[18:25], v[198:205], 0, v234, v235 op_sel_hi:[0,0,0]
	v_mfma_scale_f32_16x16x128_f8f6f4 v[90:93], v[26:33], v[198:205], 0, v234, v235 op_sel_hi:[0,0,0]
	v_mfma_scale_f32_16x16x128_f8f6f4 v[86:89], v[18:25], v[206:213], 0, v234, v235 op_sel_hi:[0,0,0]
	v_mfma_scale_f32_16x16x128_f8f6f4 v[82:85], v[26:33], v[206:213], 0, v234, v235 op_sel_hi:[0,0,0]
	s_setprio 0
	s_setprio 1
	v_mfma_scale_f32_16x16x128_f8f6f4 v[78:81], v[18:25], v[216:223], 0, v234, v235 op_sel_hi:[0,0,0]
	v_mfma_scale_f32_16x16x128_f8f6f4 v[74:77], v[26:33], v[216:223], 0, v234, v235 op_sel_hi:[0,0,0]
	v_mfma_scale_f32_16x16x128_f8f6f4 v[70:73], v[18:25], v[224:231], 0, v234, v235 op_sel_hi:[0,0,0]
	v_mfma_scale_f32_16x16x128_f8f6f4 v[66:69], v[26:33], v[224:231], 0, v234, v235 op_sel_hi:[0,0,0]
	s_setprio 0
	s_setprio 1
	v_mfma_scale_f32_16x16x128_f8f6f4 v[62:65], v[2:9], v[198:205], 0, v234, v235 op_sel_hi:[0,0,0]
	v_mfma_scale_f32_16x16x128_f8f6f4 v[58:61], v[10:17], v[198:205], 0, v234, v235 op_sel_hi:[0,0,0]
	v_mfma_scale_f32_16x16x128_f8f6f4 v[54:57], v[2:9], v[206:213], 0, v234, v235 op_sel_hi:[0,0,0]
	v_mfma_scale_f32_16x16x128_f8f6f4 v[50:53], v[10:17], v[206:213], 0, v234, v235 op_sel_hi:[0,0,0]
	s_setprio 0
	s_setprio 1
	v_mfma_scale_f32_16x16x128_f8f6f4 v[46:49], v[2:9], v[216:223], 0, v234, v235 op_sel_hi:[0,0,0]
	v_mfma_scale_f32_16x16x128_f8f6f4 v[42:45], v[10:17], v[216:223], 0, v234, v235 op_sel_hi:[0,0,0]
	v_mfma_scale_f32_16x16x128_f8f6f4 v[38:41], v[2:9], v[224:231], 0, v234, v235 op_sel_hi:[0,0,0]
	v_mfma_scale_f32_16x16x128_f8f6f4 v[34:37], v[10:17], v[224:231], 0, v234, v235 op_sel_hi:[0,0,0]
	s_setprio 0
	s_barrier
	ds_read_b128 v[18:21], v188
	ds_read_b128 v[22:25], v189
	ds_read_b128 v[26:29], v190
	ds_read_b128 v[30:33], v191
	ds_read_b128 v[2:5], v192
	ds_read_b128 v[6:9], v193
	ds_read_b128 v[10:13], v194
	ds_read_b128 v[14:17], v195
	s_add_u32 s48, s46, 0x20100
	s_addc_u32 s49, s47, 0
	s_mov_b32 m0, s63
	v_lshl_add_u64 v[232:233], s[48:49], 0, v[162:163]
	ds_read_b128 v[198:201], v196 offset:32768
	ds_read_b128 v[202:205], v196 offset:33792
	ds_read_b128 v[206:209], v196 offset:34816
	ds_read_b128 v[210:213], v196 offset:35840
	ds_read_b128 v[216:219], v196 offset:36864
	ds_read_b128 v[220:223], v196 offset:37888
	ds_read_b128 v[224:227], v196 offset:38912
	ds_read_b128 v[228:231], v196 offset:39936
	global_load_lds_dwordx4 v[232:233], off
	v_lshl_add_u64 v[232:233], s[48:49], 0, v[164:165]
	s_mov_b32 m0, s64
	s_nop 0
	global_load_lds_dwordx4 v[232:233], off
	s_waitcnt vmcnt(8)
	s_waitcnt lgkmcnt(0)
	s_barrier
	s_setprio 1
	s_waitcnt lgkmcnt(0)
	v_mfma_scale_f32_16x16x128_f8f6f4 v[158:161], v[18:25], v[198:205], v[158:161], v234, v235 op_sel_hi:[0,0,0]
	v_mfma_scale_f32_16x16x128_f8f6f4 v[154:157], v[26:33], v[198:205], v[154:157], v234, v235 op_sel_hi:[0,0,0]
	v_mfma_scale_f32_16x16x128_f8f6f4 v[150:153], v[18:25], v[206:213], v[150:153], v234, v235 op_sel_hi:[0,0,0]
	v_mfma_scale_f32_16x16x128_f8f6f4 v[146:149], v[26:33], v[206:213], v[146:149], v234, v235 op_sel_hi:[0,0,0]
	s_setprio 0
	s_setprio 1
	v_mfma_scale_f32_16x16x128_f8f6f4 v[142:145], v[18:25], v[216:223], v[142:145], v234, v235 op_sel_hi:[0,0,0]
	v_mfma_scale_f32_16x16x128_f8f6f4 v[138:141], v[26:33], v[216:223], v[138:141], v234, v235 op_sel_hi:[0,0,0]
	v_mfma_scale_f32_16x16x128_f8f6f4 v[134:137], v[18:25], v[224:231], v[134:137], v234, v235 op_sel_hi:[0,0,0]
	v_mfma_scale_f32_16x16x128_f8f6f4 v[130:133], v[26:33], v[224:231], v[130:133], v234, v235 op_sel_hi:[0,0,0]
	s_setprio 0
	s_setprio 1
	v_mfma_scale_f32_16x16x128_f8f6f4 v[126:129], v[2:9], v[198:205], v[126:129], v234, v235 op_sel_hi:[0,0,0]
	v_mfma_scale_f32_16x16x128_f8f6f4 v[122:125], v[10:17], v[198:205], v[122:125], v234, v235 op_sel_hi:[0,0,0]
	v_mfma_scale_f32_16x16x128_f8f6f4 v[118:121], v[2:9], v[206:213], v[118:121], v234, v235 op_sel_hi:[0,0,0]
	v_mfma_scale_f32_16x16x128_f8f6f4 v[114:117], v[10:17], v[206:213], v[114:117], v234, v235 op_sel_hi:[0,0,0]
	s_setprio 0
	s_setprio 1
	v_mfma_scale_f32_16x16x128_f8f6f4 v[110:113], v[2:9], v[216:223], v[110:113], v234, v235 op_sel_hi:[0,0,0]
	v_mfma_scale_f32_16x16x128_f8f6f4 v[106:109], v[10:17], v[216:223], v[106:109], v234, v235 op_sel_hi:[0,0,0]
	v_mfma_scale_f32_16x16x128_f8f6f4 v[102:105], v[2:9], v[224:231], v[102:105], v234, v235 op_sel_hi:[0,0,0]
	v_mfma_scale_f32_16x16x128_f8f6f4 v[98:101], v[10:17], v[224:231], v[98:101], v234, v235 op_sel_hi:[0,0,0]
	s_setprio 0
	s_barrier
	s_mov_b64 s[74:75], 0x180
	s_mov_b32 m0, s7
	v_lshl_add_u64 v[172:173], v[172:173], 0, s[74:75]
	s_add_u32 s48, s44, 0x20180
	ds_read_b128 v[198:201], v196 offset:49152
	ds_read_b128 v[202:205], v196 offset:50176
	ds_read_b128 v[206:209], v196 offset:51200
	ds_read_b128 v[210:213], v196 offset:52224
	ds_read_b128 v[216:219], v196 offset:53248
	ds_read_b128 v[220:223], v196 offset:54272
	ds_read_b128 v[224:227], v196 offset:55296
	ds_read_b128 v[228:231], v196 offset:56320
	global_load_lds_dwordx4 v[172:173], off
	v_lshl_add_u64 v[172:173], v[174:175], 0, s[74:75]
	s_mov_b32 m0, s65
	s_addc_u32 s49, s45, 0
	global_load_lds_dwordx4 v[172:173], off
	v_lshl_add_u64 v[172:173], s[48:49], 0, v[0:1]
	s_mov_b32 m0, s13
	s_nop 0
	global_load_lds_dwordx4 v[172:173], off
	v_lshl_add_u64 v[172:173], s[48:49], 0, v[166:167]
	s_mov_b32 m0, s51
	s_nop 0
	global_load_lds_dwordx4 v[172:173], off
	v_lshl_add_u64 v[172:173], v[176:177], 0, s[74:75]
	s_mov_b32 m0, s68
	s_nop 0
	global_load_lds_dwordx4 v[172:173], off
	v_lshl_add_u64 v[172:173], v[178:179], 0, s[74:75]
	s_mov_b32 m0, s52
	s_nop 0
	global_load_lds_dwordx4 v[172:173], off
	s_waitcnt vmcnt(8)
	s_waitcnt lgkmcnt(0)
	s_barrier
	s_setprio 1
	s_waitcnt lgkmcnt(0)
	v_mfma_scale_f32_16x16x128_f8f6f4 v[94:97], v[18:25], v[198:205], v[94:97], v234, v235 op_sel_hi:[0,0,0]
	v_mfma_scale_f32_16x16x128_f8f6f4 v[90:93], v[26:33], v[198:205], v[90:93], v234, v235 op_sel_hi:[0,0,0]
	v_mfma_scale_f32_16x16x128_f8f6f4 v[86:89], v[18:25], v[206:213], v[86:89], v234, v235 op_sel_hi:[0,0,0]
	v_mfma_scale_f32_16x16x128_f8f6f4 v[82:85], v[26:33], v[206:213], v[82:85], v234, v235 op_sel_hi:[0,0,0]
	s_setprio 0
	s_setprio 1
	v_mfma_scale_f32_16x16x128_f8f6f4 v[78:81], v[18:25], v[216:223], v[78:81], v234, v235 op_sel_hi:[0,0,0]
	v_mfma_scale_f32_16x16x128_f8f6f4 v[74:77], v[26:33], v[216:223], v[74:77], v234, v235 op_sel_hi:[0,0,0]
	v_mfma_scale_f32_16x16x128_f8f6f4 v[70:73], v[18:25], v[224:231], v[70:73], v234, v235 op_sel_hi:[0,0,0]
	v_mfma_scale_f32_16x16x128_f8f6f4 v[66:69], v[26:33], v[224:231], v[66:69], v234, v235 op_sel_hi:[0,0,0]
	s_setprio 0
	s_setprio 1
	v_mfma_scale_f32_16x16x128_f8f6f4 v[62:65], v[2:9], v[198:205], v[62:65], v234, v235 op_sel_hi:[0,0,0]
	v_mfma_scale_f32_16x16x128_f8f6f4 v[58:61], v[10:17], v[198:205], v[58:61], v234, v235 op_sel_hi:[0,0,0]
	v_mfma_scale_f32_16x16x128_f8f6f4 v[54:57], v[2:9], v[206:213], v[54:57], v234, v235 op_sel_hi:[0,0,0]
	v_mfma_scale_f32_16x16x128_f8f6f4 v[50:53], v[10:17], v[206:213], v[50:53], v234, v235 op_sel_hi:[0,0,0]
	s_setprio 0
	s_setprio 1
	v_mfma_scale_f32_16x16x128_f8f6f4 v[46:49], v[2:9], v[216:223], v[46:49], v234, v235 op_sel_hi:[0,0,0]
	v_mfma_scale_f32_16x16x128_f8f6f4 v[42:45], v[10:17], v[216:223], v[42:45], v234, v235 op_sel_hi:[0,0,0]
	v_mfma_scale_f32_16x16x128_f8f6f4 v[38:41], v[2:9], v[224:231], v[38:41], v234, v235 op_sel_hi:[0,0,0]
	v_mfma_scale_f32_16x16x128_f8f6f4 v[34:37], v[10:17], v[224:231], v[34:37], v234, v235 op_sel_hi:[0,0,0]
	s_setprio 0
	s_barrier
	s_add_u32 s46, s46, 0x20180
	s_addc_u32 s47, s47, 0
	s_add_u32 s37, s44, 0x200
	s_addc_u32 s74, s45, 0
	s_mov_b32 s75, 0
.LBB0_388:
	ds_read_b128 v[2:5], v180
	ds_read_b128 v[6:9], v181
	ds_read_b128 v[10:13], v182
	ds_read_b128 v[14:17], v183
	ds_read_b128 v[26:29], v184
	ds_read_b128 v[30:33], v185
	ds_read_b128 v[172:175], v186
	ds_read_b128 v[176:179], v187
	s_add_u32 s44, s46, 0xfffe0080
	s_addc_u32 s45, s47, -1
	s_cmp_eq_u32 s75, 4
	s_cselect_b32 s49, s1, s45
	s_cselect_b32 s48, s5, s44
	s_cselect_b32 s45, s23, s74
	s_cselect_b32 s44, s26, s37
	s_mov_b32 m0, s27
	v_lshl_add_u64 v[224:225], s[46:47], 0, v[168:169]
	ds_read_b128 v[18:21], v196
	ds_read_b128 v[22:25], v196 offset:1024
	ds_read_b128 v[198:201], v196 offset:2048
	ds_read_b128 v[202:205], v196 offset:3072
	ds_read_b128 v[206:209], v196 offset:4096
	ds_read_b128 v[210:213], v196 offset:5120
	ds_read_b128 v[216:219], v196 offset:6144
	ds_read_b128 v[220:223], v196 offset:7168
	global_load_lds_dwordx4 v[224:225], off
	v_lshl_add_u64 v[224:225], s[46:47], 0, v[170:171]
	s_mov_b32 m0, s35
	s_nop 0
	global_load_lds_dwordx4 v[224:225], off
	s_waitcnt vmcnt(8)
	s_waitcnt lgkmcnt(0)
	s_barrier
	s_setprio 1
	s_waitcnt lgkmcnt(0)
	v_mfma_scale_f32_16x16x128_f8f6f4 v[158:161], v[2:9], v[18:25], v[158:161], v234, v235 op_sel_hi:[0,0,0]
	v_mfma_scale_f32_16x16x128_f8f6f4 v[154:157], v[10:17], v[18:25], v[154:157], v234, v235 op_sel_hi:[0,0,0]
	v_mfma_scale_f32_16x16x128_f8f6f4 v[150:153], v[2:9], v[198:205], v[150:153], v234, v235 op_sel_hi:[0,0,0]
	v_mfma_scale_f32_16x16x128_f8f6f4 v[146:149], v[10:17], v[198:205], v[146:149], v234, v235 op_sel_hi:[0,0,0]
	s_setprio 0
	s_setprio 1
	v_mfma_scale_f32_16x16x128_f8f6f4 v[142:145], v[2:9], v[206:213], v[142:145], v234, v235 op_sel_hi:[0,0,0]
	v_mfma_scale_f32_16x16x128_f8f6f4 v[138:141], v[10:17], v[206:213], v[138:141], v234, v235 op_sel_hi:[0,0,0]
	v_mfma_scale_f32_16x16x128_f8f6f4 v[134:137], v[2:9], v[216:223], v[134:137], v234, v235 op_sel_hi:[0,0,0]
	v_mfma_scale_f32_16x16x128_f8f6f4 v[130:133], v[10:17], v[216:223], v[130:133], v234, v235 op_sel_hi:[0,0,0]
	s_setprio 0
	s_setprio 1
	v_mfma_scale_f32_16x16x128_f8f6f4 v[126:129], v[26:33], v[18:25], v[126:129], v234, v235 op_sel_hi:[0,0,0]
	v_mfma_scale_f32_16x16x128_f8f6f4 v[122:125], v[172:179], v[18:25], v[122:125], v234, v235 op_sel_hi:[0,0,0]
	v_mfma_scale_f32_16x16x128_f8f6f4 v[118:121], v[26:33], v[198:205], v[118:121], v234, v235 op_sel_hi:[0,0,0]
	v_mfma_scale_f32_16x16x128_f8f6f4 v[114:117], v[172:179], v[198:205], v[114:117], v234, v235 op_sel_hi:[0,0,0]
	s_setprio 0
	s_setprio 1
	v_mfma_scale_f32_16x16x128_f8f6f4 v[110:113], v[26:33], v[206:213], v[110:113], v234, v235 op_sel_hi:[0,0,0]
	v_mfma_scale_f32_16x16x128_f8f6f4 v[106:109], v[172:179], v[206:213], v[106:109], v234, v235 op_sel_hi:[0,0,0]
	v_mfma_scale_f32_16x16x128_f8f6f4 v[102:105], v[26:33], v[216:223], v[102:105], v234, v235 op_sel_hi:[0,0,0]
	v_mfma_scale_f32_16x16x128_f8f6f4 v[98:101], v[172:179], v[216:223], v[98:101], v234, v235 op_sel_hi:[0,0,0]
	s_setprio 0
	s_barrier
	s_mov_b32 m0, s58
	v_lshl_add_u64 v[18:19], s[44:45], 0, v[0:1]
	s_add_u32 vcc_lo, s44, 0x20000
	ds_read_b128 v[198:201], v196 offset:16384
	ds_read_b128 v[202:205], v196 offset:17408
	ds_read_b128 v[206:209], v196 offset:18432
	ds_read_b128 v[210:213], v196 offset:19456
	ds_read_b128 v[216:219], v196 offset:20480
	ds_read_b128 v[220:223], v196 offset:21504
	ds_read_b128 v[224:227], v196 offset:22528
	ds_read_b128 v[228:231], v196 offset:23552
	global_load_lds_dwordx4 v[18:19], off
	v_lshl_add_u64 v[20:21], s[44:45], 0, v[166:167]
	s_mov_b32 m0, s59
	s_addc_u32 vcc_hi, s45, 0
	global_load_lds_dwordx4 v[20:21], off
	v_lshl_add_u64 v[22:23], vcc, 0, v[0:1]
	s_mov_b32 m0, s60
	v_lshl_add_u64 v[24:25], s[48:49], 0, v[164:165]
	global_load_lds_dwordx4 v[22:23], off
	v_lshl_add_u64 v[22:23], vcc, 0, v[166:167]
	s_mov_b32 m0, s61
	s_nop 0
	global_load_lds_dwordx4 v[22:23], off
	v_lshl_add_u64 v[22:23], s[48:49], 0, v[162:163]
	s_mov_b32 m0, s57
	s_nop 0
	global_load_lds_dwordx4 v[22:23], off
	s_mov_b32 m0, s62
	s_nop 0
	global_load_lds_dwordx4 v[24:25], off
	s_waitcnt vmcnt(8)
	s_waitcnt lgkmcnt(0)
	s_barrier
	s_setprio 1
	s_waitcnt lgkmcnt(0)
	v_mfma_scale_f32_16x16x128_f8f6f4 v[94:97], v[2:9], v[198:205], v[94:97], v234, v235 op_sel_hi:[0,0,0]
	v_mfma_scale_f32_16x16x128_f8f6f4 v[90:93], v[10:17], v[198:205], v[90:93], v234, v235 op_sel_hi:[0,0,0]
	v_mfma_scale_f32_16x16x128_f8f6f4 v[86:89], v[2:9], v[206:213], v[86:89], v234, v235 op_sel_hi:[0,0,0]
	v_mfma_scale_f32_16x16x128_f8f6f4 v[82:85], v[10:17], v[206:213], v[82:85], v234, v235 op_sel_hi:[0,0,0]
	s_setprio 0
	s_setprio 1
	v_mfma_scale_f32_16x16x128_f8f6f4 v[78:81], v[2:9], v[216:223], v[78:81], v234, v235 op_sel_hi:[0,0,0]
	v_mfma_scale_f32_16x16x128_f8f6f4 v[74:77], v[10:17], v[216:223], v[74:77], v234, v235 op_sel_hi:[0,0,0]
	v_mfma_scale_f32_16x16x128_f8f6f4 v[70:73], v[2:9], v[224:231], v[70:73], v234, v235 op_sel_hi:[0,0,0]
	v_mfma_scale_f32_16x16x128_f8f6f4 v[66:69], v[10:17], v[224:231], v[66:69], v234, v235 op_sel_hi:[0,0,0]
	s_setprio 0
	s_setprio 1
	v_mfma_scale_f32_16x16x128_f8f6f4 v[62:65], v[26:33], v[198:205], v[62:65], v234, v235 op_sel_hi:[0,0,0]
	v_mfma_scale_f32_16x16x128_f8f6f4 v[58:61], v[172:179], v[198:205], v[58:61], v234, v235 op_sel_hi:[0,0,0]
	v_mfma_scale_f32_16x16x128_f8f6f4 v[54:57], v[26:33], v[206:213], v[54:57], v234, v235 op_sel_hi:[0,0,0]
	v_mfma_scale_f32_16x16x128_f8f6f4 v[50:53], v[172:179], v[206:213], v[50:53], v234, v235 op_sel_hi:[0,0,0]
	s_setprio 0
	s_setprio 1
	v_mfma_scale_f32_16x16x128_f8f6f4 v[46:49], v[26:33], v[216:223], v[46:49], v234, v235 op_sel_hi:[0,0,0]
	v_mfma_scale_f32_16x16x128_f8f6f4 v[42:45], v[172:179], v[216:223], v[42:45], v234, v235 op_sel_hi:[0,0,0]
	v_mfma_scale_f32_16x16x128_f8f6f4 v[38:41], v[26:33], v[224:231], v[38:41], v234, v235 op_sel_hi:[0,0,0]
	v_mfma_scale_f32_16x16x128_f8f6f4 v[34:37], v[172:179], v[224:231], v[34:37], v234, v235 op_sel_hi:[0,0,0]
	s_setprio 0
	s_barrier
	ds_read_b128 v[10:13], v188
	ds_read_b128 v[14:17], v189
	ds_read_b128 v[26:29], v190
	ds_read_b128 v[30:33], v191
	ds_read_b128 v[2:5], v192
	ds_read_b128 v[6:9], v193
	ds_read_b128 v[172:175], v194
	ds_read_b128 v[176:179], v195
	s_add_u32 s48, s48, 0x20000
	s_addc_u32 s49, s49, 0
	s_mov_b32 m0, s63
	v_lshl_add_u64 v[232:233], s[48:49], 0, v[162:163]
	ds_read_b128 v[198:201], v196 offset:32768
	ds_read_b128 v[202:205], v196 offset:33792
	ds_read_b128 v[206:209], v196 offset:34816
	ds_read_b128 v[210:213], v196 offset:35840
	ds_read_b128 v[216:219], v196 offset:36864
	ds_read_b128 v[220:223], v196 offset:37888
	ds_read_b128 v[224:227], v196 offset:38912
	ds_read_b128 v[228:231], v196 offset:39936
	global_load_lds_dwordx4 v[232:233], off
	v_lshl_add_u64 v[232:233], s[48:49], 0, v[164:165]
	s_mov_b32 m0, s64
	s_nop 0
	global_load_lds_dwordx4 v[232:233], off
	s_waitcnt vmcnt(8)
	s_waitcnt lgkmcnt(0)
	s_barrier
	s_setprio 1
	s_waitcnt lgkmcnt(0)
	v_mfma_scale_f32_16x16x128_f8f6f4 v[158:161], v[10:17], v[198:205], v[158:161], v234, v235 op_sel_hi:[0,0,0]
	v_mfma_scale_f32_16x16x128_f8f6f4 v[154:157], v[26:33], v[198:205], v[154:157], v234, v235 op_sel_hi:[0,0,0]
	v_mfma_scale_f32_16x16x128_f8f6f4 v[150:153], v[10:17], v[206:213], v[150:153], v234, v235 op_sel_hi:[0,0,0]
	v_mfma_scale_f32_16x16x128_f8f6f4 v[146:149], v[26:33], v[206:213], v[146:149], v234, v235 op_sel_hi:[0,0,0]
	s_setprio 0
	s_setprio 1
	v_mfma_scale_f32_16x16x128_f8f6f4 v[142:145], v[10:17], v[216:223], v[142:145], v234, v235 op_sel_hi:[0,0,0]
	v_mfma_scale_f32_16x16x128_f8f6f4 v[138:141], v[26:33], v[216:223], v[138:141], v234, v235 op_sel_hi:[0,0,0]
	v_mfma_scale_f32_16x16x128_f8f6f4 v[134:137], v[10:17], v[224:231], v[134:137], v234, v235 op_sel_hi:[0,0,0]
	v_mfma_scale_f32_16x16x128_f8f6f4 v[130:133], v[26:33], v[224:231], v[130:133], v234, v235 op_sel_hi:[0,0,0]
	s_setprio 0
	s_setprio 1
	v_mfma_scale_f32_16x16x128_f8f6f4 v[126:129], v[2:9], v[198:205], v[126:129], v234, v235 op_sel_hi:[0,0,0]
	v_mfma_scale_f32_16x16x128_f8f6f4 v[122:125], v[172:179], v[198:205], v[122:125], v234, v235 op_sel_hi:[0,0,0]
	v_mfma_scale_f32_16x16x128_f8f6f4 v[118:121], v[2:9], v[206:213], v[118:121], v234, v235 op_sel_hi:[0,0,0]
	v_mfma_scale_f32_16x16x128_f8f6f4 v[114:117], v[172:179], v[206:213], v[114:117], v234, v235 op_sel_hi:[0,0,0]
	s_setprio 0
	s_setprio 1
	v_mfma_scale_f32_16x16x128_f8f6f4 v[110:113], v[2:9], v[216:223], v[110:113], v234, v235 op_sel_hi:[0,0,0]
	v_mfma_scale_f32_16x16x128_f8f6f4 v[106:109], v[172:179], v[216:223], v[106:109], v234, v235 op_sel_hi:[0,0,0]
	v_mfma_scale_f32_16x16x128_f8f6f4 v[102:105], v[2:9], v[224:231], v[102:105], v234, v235 op_sel_hi:[0,0,0]
	v_mfma_scale_f32_16x16x128_f8f6f4 v[98:101], v[172:179], v[224:231], v[98:101], v234, v235 op_sel_hi:[0,0,0]
	s_setprio 0
	s_barrier
	s_mov_b32 m0, s7
	v_lshl_add_u64 v[18:19], v[18:19], 0, s[66:67]
	s_add_u32 s44, s44, 0x20080
	ds_read_b128 v[198:201], v196 offset:49152
	ds_read_b128 v[202:205], v196 offset:50176
	ds_read_b128 v[206:209], v196 offset:51200
	ds_read_b128 v[210:213], v196 offset:52224
	ds_read_b128 v[216:219], v196 offset:53248
	ds_read_b128 v[220:223], v196 offset:54272
	ds_read_b128 v[224:227], v196 offset:55296
	ds_read_b128 v[228:231], v196 offset:56320
	global_load_lds_dwordx4 v[18:19], off
	v_lshl_add_u64 v[18:19], v[20:21], 0, s[66:67]
	s_mov_b32 m0, s65
	s_addc_u32 s45, s45, 0
	global_load_lds_dwordx4 v[18:19], off
	v_lshl_add_u64 v[18:19], s[44:45], 0, v[0:1]
	s_mov_b32 m0, s13
	s_nop 0
	global_load_lds_dwordx4 v[18:19], off
	v_lshl_add_u64 v[18:19], s[44:45], 0, v[166:167]
	s_mov_b32 m0, s51
	s_nop 0
	global_load_lds_dwordx4 v[18:19], off
	v_lshl_add_u64 v[18:19], v[22:23], 0, s[66:67]
	s_mov_b32 m0, s68
	s_nop 0
	global_load_lds_dwordx4 v[18:19], off
	v_lshl_add_u64 v[18:19], v[24:25], 0, s[66:67]
	s_mov_b32 m0, s52
	s_nop 0
	global_load_lds_dwordx4 v[18:19], off
	s_waitcnt vmcnt(8)
	s_waitcnt lgkmcnt(0)
	s_barrier
	s_setprio 1
	s_waitcnt lgkmcnt(0)
	v_mfma_scale_f32_16x16x128_f8f6f4 v[94:97], v[10:17], v[198:205], v[94:97], v234, v235 op_sel_hi:[0,0,0]
	v_mfma_scale_f32_16x16x128_f8f6f4 v[90:93], v[26:33], v[198:205], v[90:93], v234, v235 op_sel_hi:[0,0,0]
	v_mfma_scale_f32_16x16x128_f8f6f4 v[86:89], v[10:17], v[206:213], v[86:89], v234, v235 op_sel_hi:[0,0,0]
	v_mfma_scale_f32_16x16x128_f8f6f4 v[82:85], v[26:33], v[206:213], v[82:85], v234, v235 op_sel_hi:[0,0,0]
	s_setprio 0
	s_setprio 1
	v_mfma_scale_f32_16x16x128_f8f6f4 v[78:81], v[10:17], v[216:223], v[78:81], v234, v235 op_sel_hi:[0,0,0]
	v_mfma_scale_f32_16x16x128_f8f6f4 v[74:77], v[26:33], v[216:223], v[74:77], v234, v235 op_sel_hi:[0,0,0]
	v_mfma_scale_f32_16x16x128_f8f6f4 v[70:73], v[10:17], v[224:231], v[70:73], v234, v235 op_sel_hi:[0,0,0]
	v_mfma_scale_f32_16x16x128_f8f6f4 v[66:69], v[26:33], v[224:231], v[66:69], v234, v235 op_sel_hi:[0,0,0]
	s_setprio 0
	s_setprio 1
	v_mfma_scale_f32_16x16x128_f8f6f4 v[62:65], v[2:9], v[198:205], v[62:65], v234, v235 op_sel_hi:[0,0,0]
	v_mfma_scale_f32_16x16x128_f8f6f4 v[58:61], v[172:179], v[198:205], v[58:61], v234, v235 op_sel_hi:[0,0,0]
	v_mfma_scale_f32_16x16x128_f8f6f4 v[54:57], v[2:9], v[206:213], v[54:57], v234, v235 op_sel_hi:[0,0,0]
	v_mfma_scale_f32_16x16x128_f8f6f4 v[50:53], v[172:179], v[206:213], v[50:53], v234, v235 op_sel_hi:[0,0,0]
	s_setprio 0
	s_setprio 1
	v_mfma_scale_f32_16x16x128_f8f6f4 v[46:49], v[2:9], v[216:223], v[46:49], v234, v235 op_sel_hi:[0,0,0]
	v_mfma_scale_f32_16x16x128_f8f6f4 v[42:45], v[172:179], v[216:223], v[42:45], v234, v235 op_sel_hi:[0,0,0]
	v_mfma_scale_f32_16x16x128_f8f6f4 v[38:41], v[2:9], v[224:231], v[38:41], v234, v235 op_sel_hi:[0,0,0]
	v_mfma_scale_f32_16x16x128_f8f6f4 v[34:37], v[172:179], v[224:231], v[34:37], v234, v235 op_sel_hi:[0,0,0]
	s_setprio 0
	s_barrier
	s_add_i32 s75, s75, 2
	s_add_u32 s46, s46, 0x100
	s_addc_u32 s47, s47, 0
	s_add_u32 s37, s37, 0x100
	s_addc_u32 s74, s74, 0
	s_cmp_gt_u32 s75, 5
	s_cbranch_scc0 .LBB0_388
	s_and_b64 vcc, exec, s[30:31]
	s_cbranch_vccz .LBB0_391
	s_barrier

.LBB0_1368:
	v_add_u32_e32 v134, 0x10000, v226
	v_add_u32_e32 v146, 0x14000, v226
	ds_read_b128 v[150:153], v134
	ds_read_b128 v[154:157], v134 offset:1024
	ds_read_b128 v[158:161], v134 offset:2048
	ds_read_b128 v[162:165], v134 offset:3072
	s_waitcnt vmcnt(0)
	ds_read_b128 v[134:137], v146
	ds_read_b128 v[138:141], v146 offset:1024
	ds_read_b128 v[142:145], v146 offset:2048
	ds_read_b128 v[146:149], v146 offset:3072
	v_lshl_add_u64 v[208:209], s[44:45], 0, v[204:205]
	s_add_i32 m0, s52, 0xc000
	s_waitcnt lgkmcnt(0)
	ds_read_b128 v[178:181], v227
	ds_read_b128 v[194:197], v227 offset:1024
	ds_read_b128 v[174:177], v227 offset:2048
	ds_read_b128 v[190:193], v227 offset:3072
	ds_read_b128 v[170:173], v227 offset:4096
	ds_read_b128 v[186:189], v227 offset:5120
	ds_read_b128 v[166:169], v227 offset:6144
	ds_read_b128 v[182:185], v227 offset:7168
	global_load_lds_dwordx4 v[208:209], off
	v_lshl_add_u64 v[208:209], s[44:45], 0, v[206:207]
	s_add_i32 m0, s52, 0xe000
	s_nop 0
	global_load_lds_dwordx4 v[208:209], off
	s_waitcnt vmcnt(8)
	s_waitcnt lgkmcnt(0)
	s_barrier
	s_setprio 1
	s_waitcnt lgkmcnt(0)
	v_mfma_f32_16x16x32_bf16 v[130:133], v[150:153], v[178:181], v[130:133]
	v_mfma_f32_16x16x32_bf16 v[126:129], v[158:161], v[178:181], v[126:129]
	v_mfma_f32_16x16x32_bf16 v[122:125], v[150:153], v[174:177], v[122:125]
	v_mfma_f32_16x16x32_bf16 v[118:121], v[158:161], v[174:177], v[118:121]
	v_mfma_f32_16x16x32_bf16 v[114:117], v[150:153], v[170:173], v[114:117]
	v_mfma_f32_16x16x32_bf16 v[110:113], v[158:161], v[170:173], v[110:113]
	v_mfma_f32_16x16x32_bf16 v[106:109], v[150:153], v[166:169], v[106:109]
	v_mfma_f32_16x16x32_bf16 v[102:105], v[158:161], v[166:169], v[102:105]
	s_setprio 0
	s_setprio 1
	v_mfma_f32_16x16x32_bf16 v[130:133], v[154:157], v[194:197], v[130:133]
	v_mfma_f32_16x16x32_bf16 v[126:129], v[162:165], v[194:197], v[126:129]
	v_mfma_f32_16x16x32_bf16 v[122:125], v[154:157], v[190:193], v[122:125]
	v_mfma_f32_16x16x32_bf16 v[118:121], v[162:165], v[190:193], v[118:121]
	v_mfma_f32_16x16x32_bf16 v[114:117], v[154:157], v[186:189], v[114:117]
	v_mfma_f32_16x16x32_bf16 v[110:113], v[162:165], v[186:189], v[110:113]
	v_mfma_f32_16x16x32_bf16 v[106:109], v[154:157], v[182:185], v[106:109]
	v_mfma_f32_16x16x32_bf16 v[102:105], v[162:165], v[182:185], v[102:105]
	s_setprio 0
	s_setprio 1
	v_mfma_f32_16x16x32_bf16 v[98:101], v[134:137], v[178:181], v[98:101]
	v_mfma_f32_16x16x32_bf16 v[94:97], v[142:145], v[178:181], v[94:97]
	v_mfma_f32_16x16x32_bf16 v[90:93], v[134:137], v[174:177], v[90:93]
	v_mfma_f32_16x16x32_bf16 v[86:89], v[142:145], v[174:177], v[86:89]
	v_mfma_f32_16x16x32_bf16 v[82:85], v[134:137], v[170:173], v[82:85]
	v_mfma_f32_16x16x32_bf16 v[78:81], v[142:145], v[170:173], v[78:81]
	v_mfma_f32_16x16x32_bf16 v[74:77], v[134:137], v[166:169], v[74:77]
	v_mfma_f32_16x16x32_bf16 v[70:73], v[142:145], v[166:169], v[70:73]
	s_setprio 0
	s_setprio 1
	v_mfma_f32_16x16x32_bf16 v[98:101], v[138:141], v[194:197], v[98:101]
	v_mfma_f32_16x16x32_bf16 v[94:97], v[146:149], v[194:197], v[94:97]
	v_mfma_f32_16x16x32_bf16 v[90:93], v[138:141], v[190:193], v[90:93]
	v_mfma_f32_16x16x32_bf16 v[86:89], v[146:149], v[190:193], v[86:89]
	v_mfma_f32_16x16x32_bf16 v[82:85], v[138:141], v[186:189], v[82:85]
	v_mfma_f32_16x16x32_bf16 v[78:81], v[146:149], v[186:189], v[78:81]
	v_mfma_f32_16x16x32_bf16 v[74:77], v[138:141], v[182:185], v[74:77]
	v_mfma_f32_16x16x32_bf16 v[70:73], v[146:149], v[182:185], v[70:73]
	s_setprio 0
	s_barrier
	v_cndmask_b32_e64 v208, 0, 1, s[6:7]
	v_cmp_ne_u32_e64 s[8:9], 1, v208
	s_andn2_b64 vcc, exec, s[6:7]
	s_cbranch_vccnz .LBB0_1370
	ds_read_b128 v[178:181], v227 offset:16384
	ds_read_b128 v[194:197], v227 offset:17408
	ds_read_b128 v[174:177], v227 offset:18432
	ds_read_b128 v[190:193], v227 offset:19456
	ds_read_b128 v[170:173], v227 offset:20480
	ds_read_b128 v[186:189], v227 offset:21504
	ds_read_b128 v[166:169], v227 offset:22528
	ds_read_b128 v[182:185], v227 offset:23552
.LBB0_1370:
	s_add_u32 s46, s44, 0xfffa0080
	s_addc_u32 s47, s45, -1
	s_cmp_eq_u32 s83, 4
	s_cselect_b32 s49, s41, s47
	s_cselect_b32 s48, s40, s46
	s_cselect_b32 s47, s27, s75
	s_cselect_b32 s46, s39, s74
	s_mov_b32 m0, s53
	v_lshl_add_u64 v[208:209], s[46:47], 0, v[0:1]
	s_add_u32 vcc_lo, s46, 0x20000
	global_load_lds_dwordx4 v[208:209], off
	v_lshl_add_u64 v[210:211], s[46:47], 0, v[202:203]
	s_mov_b32 m0, s54
	s_addc_u32 vcc_hi, s47, 0
	global_load_lds_dwordx4 v[210:211], off
	v_lshl_add_u64 v[212:213], vcc, 0, v[0:1]
	s_mov_b32 m0, s55
	v_lshl_add_u64 v[216:217], s[48:49], 0, v[200:201]
	global_load_lds_dwordx4 v[212:213], off
	v_lshl_add_u64 v[212:213], vcc, 0, v[202:203]
	s_mov_b32 m0, s56
	s_and_b64 vcc, exec, s[8:9]
	global_load_lds_dwordx4 v[212:213], off
	v_lshl_add_u64 v[212:213], s[48:49], 0, v[198:199]
	s_mov_b32 m0, s52
	s_nop 0
	global_load_lds_dwordx4 v[212:213], off
	s_mov_b32 m0, s57
	s_nop 0
	global_load_lds_dwordx4 v[216:217], off
	s_waitcnt vmcnt(8)
	s_waitcnt lgkmcnt(0)
	s_barrier
	s_cbranch_vccnz .LBB0_1372
	s_setprio 1
	s_waitcnt lgkmcnt(0)
	v_mfma_f32_16x16x32_bf16 v[66:69], v[150:153], v[178:181], v[66:69]
	v_mfma_f32_16x16x32_bf16 v[62:65], v[158:161], v[178:181], v[62:65]
	v_mfma_f32_16x16x32_bf16 v[58:61], v[150:153], v[174:177], v[58:61]
	v_mfma_f32_16x16x32_bf16 v[54:57], v[158:161], v[174:177], v[54:57]
	v_mfma_f32_16x16x32_bf16 v[50:53], v[150:153], v[170:173], v[50:53]
	v_mfma_f32_16x16x32_bf16 v[46:49], v[158:161], v[170:173], v[46:49]
	v_mfma_f32_16x16x32_bf16 v[42:45], v[150:153], v[166:169], v[42:45]
	v_mfma_f32_16x16x32_bf16 v[38:41], v[158:161], v[166:169], v[38:41]
	s_setprio 0
	s_setprio 1
	v_mfma_f32_16x16x32_bf16 v[66:69], v[154:157], v[194:197], v[66:69]
	v_mfma_f32_16x16x32_bf16 v[62:65], v[162:165], v[194:197], v[62:65]
	v_mfma_f32_16x16x32_bf16 v[58:61], v[154:157], v[190:193], v[58:61]
	v_mfma_f32_16x16x32_bf16 v[54:57], v[162:165], v[190:193], v[54:57]
	v_mfma_f32_16x16x32_bf16 v[50:53], v[154:157], v[186:189], v[50:53]
	v_mfma_f32_16x16x32_bf16 v[46:49], v[162:165], v[186:189], v[46:49]
	v_mfma_f32_16x16x32_bf16 v[42:45], v[154:157], v[182:185], v[42:45]
	v_mfma_f32_16x16x32_bf16 v[38:41], v[162:165], v[182:185], v[38:41]
	s_setprio 0
	s_setprio 1
	v_mfma_f32_16x16x32_bf16 v[34:37], v[134:137], v[178:181], v[34:37]
	v_mfma_f32_16x16x32_bf16 v[30:33], v[142:145], v[178:181], v[30:33]
	v_mfma_f32_16x16x32_bf16 v[26:29], v[134:137], v[174:177], v[26:29]
	v_mfma_f32_16x16x32_bf16 v[22:25], v[142:145], v[174:177], v[22:25]
	v_mfma_f32_16x16x32_bf16 v[18:21], v[134:137], v[170:173], v[18:21]
	v_mfma_f32_16x16x32_bf16 v[14:17], v[142:145], v[170:173], v[14:17]
	v_mfma_f32_16x16x32_bf16 v[10:13], v[134:137], v[166:169], v[10:13]
	v_mfma_f32_16x16x32_bf16 v[6:9], v[142:145], v[166:169], v[6:9]
	s_setprio 0
	s_setprio 1
	v_mfma_f32_16x16x32_bf16 v[34:37], v[138:141], v[194:197], v[34:37]
	v_mfma_f32_16x16x32_bf16 v[30:33], v[146:149], v[194:197], v[30:33]
	v_mfma_f32_16x16x32_bf16 v[26:29], v[138:141], v[190:193], v[26:29]
	v_mfma_f32_16x16x32_bf16 v[22:25], v[146:149], v[190:193], v[22:25]
	v_mfma_f32_16x16x32_bf16 v[18:21], v[138:141], v[186:189], v[18:21]
	v_mfma_f32_16x16x32_bf16 v[14:17], v[146:149], v[186:189], v[14:17]
	v_mfma_f32_16x16x32_bf16 v[10:13], v[138:141], v[182:185], v[10:13]
	v_mfma_f32_16x16x32_bf16 v[6:9], v[146:149], v[182:185], v[6:9]
	s_setprio 0
.LBB0_1372:
	s_barrier
	v_add_u32_e32 v134, 0x18000, v226
	v_add_u32_e32 v146, 0x1c000, v226
	ds_read_b128 v[150:153], v134
	ds_read_b128 v[154:157], v134 offset:1024
	ds_read_b128 v[158:161], v134 offset:2048
	ds_read_b128 v[162:165], v134 offset:3072
	ds_read_b128 v[134:137], v146
	ds_read_b128 v[138:141], v146 offset:1024
	ds_read_b128 v[142:145], v146 offset:2048
	ds_read_b128 v[146:149], v146 offset:3072
	s_add_u32 s48, s48, 0x60000
	s_addc_u32 s49, s49, 0
	s_mov_b32 m0, s58
	v_lshl_add_u64 v[218:219], s[48:49], 0, v[198:199]
	s_waitcnt lgkmcnt(0)
	ds_read_b128 v[178:181], v227 offset:32768
	ds_read_b128 v[194:197], v227 offset:33792
	ds_read_b128 v[174:177], v227 offset:34816
	ds_read_b128 v[190:193], v227 offset:35840
	ds_read_b128 v[170:173], v227 offset:36864
	ds_read_b128 v[186:189], v227 offset:37888
	ds_read_b128 v[166:169], v227 offset:38912
	ds_read_b128 v[182:185], v227 offset:39936
	global_load_lds_dwordx4 v[218:219], off
	v_lshl_add_u64 v[218:219], s[48:49], 0, v[200:201]
	s_mov_b32 m0, s59
	s_nop 0
	global_load_lds_dwordx4 v[218:219], off
	s_waitcnt vmcnt(8)
	s_waitcnt lgkmcnt(0)
	s_barrier
	s_setprio 1
	s_waitcnt lgkmcnt(0)
	v_mfma_f32_16x16x32_bf16 v[130:133], v[150:153], v[178:181], v[130:133]
	v_mfma_f32_16x16x32_bf16 v[126:129], v[158:161], v[178:181], v[126:129]
	v_mfma_f32_16x16x32_bf16 v[122:125], v[150:153], v[174:177], v[122:125]
	v_mfma_f32_16x16x32_bf16 v[118:121], v[158:161], v[174:177], v[118:121]
	v_mfma_f32_16x16x32_bf16 v[114:117], v[150:153], v[170:173], v[114:117]
	v_mfma_f32_16x16x32_bf16 v[110:113], v[158:161], v[170:173], v[110:113]
	v_mfma_f32_16x16x32_bf16 v[106:109], v[150:153], v[166:169], v[106:109]
	v_mfma_f32_16x16x32_bf16 v[102:105], v[158:161], v[166:169], v[102:105]
	s_setprio 0
	s_setprio 1
	v_mfma_f32_16x16x32_bf16 v[130:133], v[154:157], v[194:197], v[130:133]
	v_mfma_f32_16x16x32_bf16 v[126:129], v[162:165], v[194:197], v[126:129]
	v_mfma_f32_16x16x32_bf16 v[122:125], v[154:157], v[190:193], v[122:125]
	v_mfma_f32_16x16x32_bf16 v[118:121], v[162:165], v[190:193], v[118:121]
	v_mfma_f32_16x16x32_bf16 v[114:117], v[154:157], v[186:189], v[114:117]
	v_mfma_f32_16x16x32_bf16 v[110:113], v[162:165], v[186:189], v[110:113]
	v_mfma_f32_16x16x32_bf16 v[106:109], v[154:157], v[182:185], v[106:109]
	v_mfma_f32_16x16x32_bf16 v[102:105], v[162:165], v[182:185], v[102:105]
	s_setprio 0
	s_setprio 1
	v_mfma_f32_16x16x32_bf16 v[98:101], v[134:137], v[178:181], v[98:101]
	v_mfma_f32_16x16x32_bf16 v[94:97], v[142:145], v[178:181], v[94:97]
	v_mfma_f32_16x16x32_bf16 v[90:93], v[134:137], v[174:177], v[90:93]
	v_mfma_f32_16x16x32_bf16 v[86:89], v[142:145], v[174:177], v[86:89]
	v_mfma_f32_16x16x32_bf16 v[82:85], v[134:137], v[170:173], v[82:85]
	v_mfma_f32_16x16x32_bf16 v[78:81], v[142:145], v[170:173], v[78:81]
	v_mfma_f32_16x16x32_bf16 v[74:77], v[134:137], v[166:169], v[74:77]
	v_mfma_f32_16x16x32_bf16 v[70:73], v[142:145], v[166:169], v[70:73]
	s_setprio 0
	s_setprio 1
	v_mfma_f32_16x16x32_bf16 v[98:101], v[138:141], v[194:197], v[98:101]
	v_mfma_f32_16x16x32_bf16 v[94:97], v[146:149], v[194:197], v[94:97]
	v_mfma_f32_16x16x32_bf16 v[90:93], v[138:141], v[190:193], v[90:93]
	v_mfma_f32_16x16x32_bf16 v[86:89], v[146:149], v[190:193], v[86:89]
	v_mfma_f32_16x16x32_bf16 v[82:85], v[138:141], v[186:189], v[82:85]
	v_mfma_f32_16x16x32_bf16 v[78:81], v[146:149], v[186:189], v[78:81]
	v_mfma_f32_16x16x32_bf16 v[74:77], v[138:141], v[182:185], v[74:77]
	v_mfma_f32_16x16x32_bf16 v[70:73], v[146:149], v[182:185], v[70:73]
	s_setprio 0
	s_barrier
	s_and_b64 vcc, exec, s[8:9]
	s_cbranch_vccnz .LBB0_1374
	ds_read_b128 v[178:181], v227 offset:49152
	ds_read_b128 v[194:197], v227 offset:50176
	ds_read_b128 v[174:177], v227 offset:51200
	ds_read_b128 v[190:193], v227 offset:52224
	ds_read_b128 v[170:173], v227 offset:53248
	ds_read_b128 v[186:189], v227 offset:54272
	ds_read_b128 v[166:169], v227 offset:55296
	ds_read_b128 v[182:185], v227 offset:56320
.LBB0_1374:
	s_mov_b32 m0, s62
	v_lshl_add_u64 v[208:209], v[208:209], 0, s[66:67]
	s_add_u32 s46, s46, 0x20080
	global_load_lds_dwordx4 v[208:209], off
	v_lshl_add_u64 v[208:209], v[210:211], 0, s[66:67]
	s_mov_b32 m0, s63
	s_addc_u32 s47, s47, 0
	global_load_lds_dwordx4 v[208:209], off
	v_lshl_add_u64 v[208:209], s[46:47], 0, v[0:1]
	s_mov_b32 m0, s68
	s_and_b64 vcc, exec, s[8:9]
	global_load_lds_dwordx4 v[208:209], off
	v_lshl_add_u64 v[208:209], s[46:47], 0, v[202:203]
	s_mov_b32 m0, s81
	s_nop 0
	global_load_lds_dwordx4 v[208:209], off
	v_lshl_add_u64 v[208:209], v[212:213], 0, s[66:67]
	s_mov_b32 m0, s64
	s_nop 0
	global_load_lds_dwordx4 v[208:209], off
	v_lshl_add_u64 v[208:209], v[216:217], 0, s[66:67]
	s_mov_b32 m0, s65
	s_nop 0
	global_load_lds_dwordx4 v[208:209], off
	s_waitcnt vmcnt(8)
	s_waitcnt lgkmcnt(0)
	s_barrier
	s_cbranch_vccnz .LBB0_1367
	s_setprio 1
	s_waitcnt lgkmcnt(0)
	v_mfma_f32_16x16x32_bf16 v[66:69], v[150:153], v[178:181], v[66:69]
	v_mfma_f32_16x16x32_bf16 v[62:65], v[158:161], v[178:181], v[62:65]
	v_mfma_f32_16x16x32_bf16 v[58:61], v[150:153], v[174:177], v[58:61]
	v_mfma_f32_16x16x32_bf16 v[54:57], v[158:161], v[174:177], v[54:57]
	v_mfma_f32_16x16x32_bf16 v[50:53], v[150:153], v[170:173], v[50:53]
	v_mfma_f32_16x16x32_bf16 v[46:49], v[158:161], v[170:173], v[46:49]
	v_mfma_f32_16x16x32_bf16 v[42:45], v[150:153], v[166:169], v[42:45]
	v_mfma_f32_16x16x32_bf16 v[38:41], v[158:161], v[166:169], v[38:41]
	s_setprio 0
	s_setprio 1
	v_mfma_f32_16x16x32_bf16 v[66:69], v[154:157], v[194:197], v[66:69]
	v_mfma_f32_16x16x32_bf16 v[62:65], v[162:165], v[194:197], v[62:65]
	v_mfma_f32_16x16x32_bf16 v[58:61], v[154:157], v[190:193], v[58:61]
	v_mfma_f32_16x16x32_bf16 v[54:57], v[162:165], v[190:193], v[54:57]
	v_mfma_f32_16x16x32_bf16 v[50:53], v[154:157], v[186:189], v[50:53]
	v_mfma_f32_16x16x32_bf16 v[46:49], v[162:165], v[186:189], v[46:49]
	v_mfma_f32_16x16x32_bf16 v[42:45], v[154:157], v[182:185], v[42:45]
	v_mfma_f32_16x16x32_bf16 v[38:41], v[162:165], v[182:185], v[38:41]
	s_setprio 0
	s_setprio 1
	v_mfma_f32_16x16x32_bf16 v[34:37], v[134:137], v[178:181], v[34:37]
	v_mfma_f32_16x16x32_bf16 v[30:33], v[142:145], v[178:181], v[30:33]
	v_mfma_f32_16x16x32_bf16 v[26:29], v[134:137], v[174:177], v[26:29]
	v_mfma_f32_16x16x32_bf16 v[22:25], v[142:145], v[174:177], v[22:25]
	v_mfma_f32_16x16x32_bf16 v[18:21], v[134:137], v[170:173], v[18:21]
	v_mfma_f32_16x16x32_bf16 v[14:17], v[142:145], v[170:173], v[14:17]
	v_mfma_f32_16x16x32_bf16 v[10:13], v[134:137], v[166:169], v[10:13]
	v_mfma_f32_16x16x32_bf16 v[6:9], v[142:145], v[166:169], v[6:9]
	s_setprio 0
	s_setprio 1
	v_mfma_f32_16x16x32_bf16 v[34:37], v[138:141], v[194:197], v[34:37]
	v_mfma_f32_16x16x32_bf16 v[30:33], v[146:149], v[194:197], v[30:33]
	v_mfma_f32_16x16x32_bf16 v[26:29], v[138:141], v[190:193], v[26:29]
	v_mfma_f32_16x16x32_bf16 v[22:25], v[146:149], v[190:193], v[22:25]
	v_mfma_f32_16x16x32_bf16 v[18:21], v[138:141], v[186:189], v[18:21]
	v_mfma_f32_16x16x32_bf16 v[14:17], v[146:149], v[186:189], v[14:17]
	v_mfma_f32_16x16x32_bf16 v[10:13], v[138:141], v[182:185], v[10:13]
	v_mfma_f32_16x16x32_bf16 v[6:9], v[146:149], v[182:185], v[6:9]
	s_setprio 0
	s_branch .LBB0_1367

.LBB0_1556:
	v_add_u32_e32 v54, 0x10000, v247
	ds_read_b128 v[166:169], v54
	ds_read_b128 v[170:173], v54 offset:1024
	ds_read_b128 v[174:177], v54 offset:2048
	ds_read_b128 v[178:181], v54 offset:3072
	v_add_u32_e32 v54, 0x14000, v247
	ds_read_b128 v[150:153], v54
	ds_read_b128 v[154:157], v54 offset:1024
	ds_read_b128 v[158:161], v54 offset:2048
	ds_read_b128 v[162:165], v54 offset:3072
	v_lshl_add_u64 v[54:55], s[40:41], 0, v[222:223]
	s_add_i32 m0, s26, 0xc000
	s_waitcnt lgkmcnt(0)
	ds_read_b128 v[194:197], v248
	ds_read_b128 v[210:213], v248 offset:1024
	ds_read_b128 v[190:193], v248 offset:2048
	ds_read_b128 v[206:209], v248 offset:3072
	ds_read_b128 v[186:189], v248 offset:4096
	ds_read_b128 v[202:205], v248 offset:5120
	ds_read_b128 v[182:185], v248 offset:6144
	ds_read_b128 v[198:201], v248 offset:7168
	global_load_lds_dwordx4 v[54:55], off
	v_lshl_add_u64 v[54:55], s[40:41], 0, v[224:225]
	s_add_i32 m0, s26, 0xe000
	s_nop 0
	global_load_lds_dwordx4 v[54:55], off
	s_waitcnt vmcnt(8)
	s_waitcnt lgkmcnt(0)
	s_barrier
	s_setprio 1
	s_waitcnt lgkmcnt(0)
	v_mfma_f32_16x16x32_bf16 v[54:57], v[166:169], v[194:197], v[146:149]
	v_mfma_f32_16x16x32_bf16 v[58:61], v[174:177], v[194:197], v[142:145]
	v_mfma_f32_16x16x32_bf16 v[66:69], v[166:169], v[190:193], v[130:133]
	v_mfma_f32_16x16x32_bf16 v[74:77], v[174:177], v[190:193], v[126:129]
	v_mfma_f32_16x16x32_bf16 v[114:117], v[166:169], v[186:189], v[114:117]
	v_mfma_f32_16x16x32_bf16 v[110:113], v[174:177], v[186:189], v[110:113]
	v_mfma_f32_16x16x32_bf16 v[98:101], v[166:169], v[182:185], v[98:101]
	v_mfma_f32_16x16x32_bf16 v[94:97], v[174:177], v[182:185], v[94:97]
	s_setprio 0
	s_setprio 1
	v_mfma_f32_16x16x32_bf16 v[54:57], v[170:173], v[210:213], v[54:57]
	v_mfma_f32_16x16x32_bf16 v[58:61], v[178:181], v[210:213], v[58:61]
	v_mfma_f32_16x16x32_bf16 v[66:69], v[170:173], v[206:209], v[66:69]
	v_mfma_f32_16x16x32_bf16 v[74:77], v[178:181], v[206:209], v[74:77]
	v_mfma_f32_16x16x32_bf16 v[114:117], v[170:173], v[202:205], v[114:117]
	v_mfma_f32_16x16x32_bf16 v[110:113], v[178:181], v[202:205], v[110:113]
	v_mfma_f32_16x16x32_bf16 v[98:101], v[170:173], v[198:201], v[98:101]
	v_mfma_f32_16x16x32_bf16 v[94:97], v[178:181], v[198:201], v[94:97]
	s_setprio 0
	s_setprio 1
	v_mfma_f32_16x16x32_bf16 v[126:129], v[150:153], v[194:197], v[138:141]
	v_mfma_f32_16x16x32_bf16 v[138:141], v[154:157], v[210:213], v[126:129]
	v_mfma_f32_16x16x32_bf16 v[126:129], v[158:161], v[194:197], v[134:137]
	v_mfma_f32_16x16x32_bf16 v[122:125], v[150:153], v[190:193], v[122:125]
	v_mfma_f32_16x16x32_bf16 v[118:121], v[158:161], v[190:193], v[118:121]
	v_mfma_f32_16x16x32_bf16 v[106:109], v[150:153], v[186:189], v[106:109]
	v_mfma_f32_16x16x32_bf16 v[102:105], v[158:161], v[186:189], v[102:105]
	v_mfma_f32_16x16x32_bf16 v[90:93], v[150:153], v[182:185], v[90:93]
	s_setprio 0
	s_setprio 1
	v_mfma_f32_16x16x32_bf16 v[86:89], v[158:161], v[182:185], v[86:89]
	v_mfma_f32_16x16x32_bf16 v[134:137], v[162:165], v[210:213], v[126:129]
	v_mfma_f32_16x16x32_bf16 v[122:125], v[154:157], v[206:209], v[122:125]
	v_mfma_f32_16x16x32_bf16 v[118:121], v[162:165], v[206:209], v[118:121]
	v_mfma_f32_16x16x32_bf16 v[106:109], v[154:157], v[202:205], v[106:109]
	v_mfma_f32_16x16x32_bf16 v[102:105], v[162:165], v[202:205], v[102:105]
	v_mfma_f32_16x16x32_bf16 v[90:93], v[154:157], v[198:201], v[90:93]
	v_mfma_f32_16x16x32_bf16 v[86:89], v[162:165], v[198:201], v[86:89]
	s_setprio 0
	s_barrier
	v_cndmask_b32_e64 v126, 0, 1, s[38:39]
	v_cmp_ne_u32_e64 s[0:1], 1, v126
	s_andn2_b64 vcc, exec, s[38:39]
	s_cbranch_vccnz .LBB0_1558
	ds_read_b128 v[194:197], v248 offset:16384
	ds_read_b128 v[210:213], v248 offset:17408
	ds_read_b128 v[190:193], v248 offset:18432
	ds_read_b128 v[206:209], v248 offset:19456
	ds_read_b128 v[186:189], v248 offset:20480
	ds_read_b128 v[202:205], v248 offset:21504
	ds_read_b128 v[182:185], v248 offset:22528
	ds_read_b128 v[198:201], v248 offset:23552
.LBB0_1558:
	s_add_u32 s42, s40, 0xfffc0080
	s_addc_u32 s43, s41, -1
	s_cmp_eq_u32 s90, 12
	s_cselect_b32 s45, s74, s43
	s_cselect_b32 s44, s75, s42
	s_cselect_b32 s43, s11, s88
	s_cselect_b32 s42, s81, s83
	s_mov_b32 m0, s27
	v_lshl_add_u64 v[226:227], s[42:43], 0, v[0:1]
	s_add_u32 vcc_lo, s42, 0x40000
	global_load_lds_dwordx4 v[226:227], off
	v_lshl_add_u64 v[228:229], s[42:43], 0, v[220:221]
	s_mov_b32 m0, s37
	s_addc_u32 vcc_hi, s43, 0
	global_load_lds_dwordx4 v[228:229], off
	v_lshl_add_u64 v[126:127], vcc, 0, v[0:1]
	s_mov_b32 m0, s47
	v_lshl_add_u64 v[230:231], s[44:45], 0, v[216:217]
	global_load_lds_dwordx4 v[126:127], off
	v_lshl_add_u64 v[126:127], vcc, 0, v[220:221]
	s_mov_b32 m0, s48
	v_lshl_add_u64 v[232:233], s[44:45], 0, v[218:219]
	global_load_lds_dwordx4 v[126:127], off
	s_mov_b32 m0, s26
	s_and_b64 vcc, exec, s[0:1]
	global_load_lds_dwordx4 v[230:231], off
	s_mov_b32 m0, s49
	s_nop 0
	global_load_lds_dwordx4 v[232:233], off
	s_waitcnt vmcnt(8)
	s_waitcnt lgkmcnt(0)
	s_barrier
	s_cbranch_vccnz .LBB0_1560
	s_setprio 1
	s_waitcnt lgkmcnt(0)
	v_mfma_f32_16x16x32_bf16 v[82:85], v[166:169], v[194:197], v[82:85]
	v_mfma_f32_16x16x32_bf16 v[78:81], v[174:177], v[194:197], v[78:81]
	v_mfma_f32_16x16x32_bf16 v[50:53], v[166:169], v[190:193], v[50:53]
	v_mfma_f32_16x16x32_bf16 v[46:49], v[174:177], v[190:193], v[46:49]
	v_mfma_f32_16x16x32_bf16 v[34:37], v[166:169], v[186:189], v[34:37]
	v_mfma_f32_16x16x32_bf16 v[30:33], v[174:177], v[186:189], v[30:33]
	v_mfma_f32_16x16x32_bf16 v[18:21], v[166:169], v[182:185], v[18:21]
	v_mfma_f32_16x16x32_bf16 v[14:17], v[174:177], v[182:185], v[14:17]
	s_setprio 0
	s_setprio 1
	v_mfma_f32_16x16x32_bf16 v[82:85], v[170:173], v[210:213], v[82:85]
	v_mfma_f32_16x16x32_bf16 v[78:81], v[178:181], v[210:213], v[78:81]
	v_mfma_f32_16x16x32_bf16 v[50:53], v[170:173], v[206:209], v[50:53]
	v_mfma_f32_16x16x32_bf16 v[46:49], v[178:181], v[206:209], v[46:49]
	v_mfma_f32_16x16x32_bf16 v[34:37], v[170:173], v[202:205], v[34:37]
	v_mfma_f32_16x16x32_bf16 v[30:33], v[178:181], v[202:205], v[30:33]
	v_mfma_f32_16x16x32_bf16 v[18:21], v[170:173], v[198:201], v[18:21]
	v_mfma_f32_16x16x32_bf16 v[14:17], v[178:181], v[198:201], v[14:17]
	s_setprio 0
	s_setprio 1
	v_mfma_f32_16x16x32_bf16 v[70:73], v[150:153], v[194:197], v[70:73]
	v_mfma_f32_16x16x32_bf16 v[62:65], v[158:161], v[194:197], v[62:65]
	v_mfma_f32_16x16x32_bf16 v[42:45], v[150:153], v[190:193], v[42:45]
	v_mfma_f32_16x16x32_bf16 v[38:41], v[158:161], v[190:193], v[38:41]
	v_mfma_f32_16x16x32_bf16 v[26:29], v[150:153], v[186:189], v[26:29]
	v_mfma_f32_16x16x32_bf16 v[22:25], v[158:161], v[186:189], v[22:25]
	v_mfma_f32_16x16x32_bf16 v[10:13], v[150:153], v[182:185], v[10:13]
	v_mfma_f32_16x16x32_bf16 v[6:9], v[158:161], v[182:185], v[6:9]
	s_setprio 0
	s_setprio 1
	v_mfma_f32_16x16x32_bf16 v[70:73], v[154:157], v[210:213], v[70:73]
	v_mfma_f32_16x16x32_bf16 v[62:65], v[162:165], v[210:213], v[62:65]
	v_mfma_f32_16x16x32_bf16 v[42:45], v[154:157], v[206:209], v[42:45]
	v_mfma_f32_16x16x32_bf16 v[38:41], v[162:165], v[206:209], v[38:41]
	v_mfma_f32_16x16x32_bf16 v[26:29], v[154:157], v[202:205], v[26:29]
	v_mfma_f32_16x16x32_bf16 v[22:25], v[162:165], v[202:205], v[22:25]
	v_mfma_f32_16x16x32_bf16 v[10:13], v[154:157], v[198:201], v[10:13]
	v_mfma_f32_16x16x32_bf16 v[6:9], v[162:165], v[198:201], v[6:9]
	s_setprio 0
.LBB0_1560:
	s_barrier
	v_add_u32_e32 v126, 0x18000, v247
	ds_read_b128 v[166:169], v126
	ds_read_b128 v[170:173], v126 offset:1024
	ds_read_b128 v[174:177], v126 offset:2048
	ds_read_b128 v[178:181], v126 offset:3072
	v_add_u32_e32 v126, 0x1c000, v247
	ds_read_b128 v[150:153], v126
	ds_read_b128 v[154:157], v126 offset:1024
	ds_read_b128 v[158:161], v126 offset:2048
	ds_read_b128 v[162:165], v126 offset:3072
	s_add_u32 s44, s44, 0x40000
	s_addc_u32 s45, s45, 0
	s_mov_b32 m0, s50
	v_lshl_add_u64 v[126:127], s[44:45], 0, v[216:217]
	s_waitcnt lgkmcnt(0)
	ds_read_b128 v[194:197], v248 offset:32768
	ds_read_b128 v[210:213], v248 offset:33792
	ds_read_b128 v[190:193], v248 offset:34816
	ds_read_b128 v[206:209], v248 offset:35840
	ds_read_b128 v[186:189], v248 offset:36864
	ds_read_b128 v[202:205], v248 offset:37888
	ds_read_b128 v[182:185], v248 offset:38912
	ds_read_b128 v[198:201], v248 offset:39936
	global_load_lds_dwordx4 v[126:127], off
	v_lshl_add_u64 v[126:127], s[44:45], 0, v[218:219]
	s_mov_b32 m0, s51
	s_nop 0
	global_load_lds_dwordx4 v[126:127], off
	s_waitcnt vmcnt(8)
	s_waitcnt lgkmcnt(0)
	s_barrier
	s_setprio 1
	s_waitcnt lgkmcnt(0)
	v_mfma_f32_16x16x32_bf16 v[54:57], v[166:169], v[194:197], v[54:57]
	v_mfma_f32_16x16x32_bf16 v[146:149], v[170:173], v[210:213], v[54:57]
	v_mfma_f32_16x16x32_bf16 v[54:57], v[174:177], v[194:197], v[58:61]
	v_mfma_f32_16x16x32_bf16 v[142:145], v[178:181], v[210:213], v[54:57]
	v_mfma_f32_16x16x32_bf16 v[54:57], v[166:169], v[190:193], v[66:69]
	v_mfma_f32_16x16x32_bf16 v[130:133], v[170:173], v[206:209], v[54:57]
	v_mfma_f32_16x16x32_bf16 v[54:57], v[174:177], v[190:193], v[74:77]
	v_mfma_f32_16x16x32_bf16 v[126:129], v[178:181], v[206:209], v[54:57]
	s_setprio 0
	s_setprio 1
	v_mfma_f32_16x16x32_bf16 v[54:57], v[166:169], v[186:189], v[114:117]
	v_mfma_f32_16x16x32_bf16 v[114:117], v[170:173], v[202:205], v[54:57]
	v_mfma_f32_16x16x32_bf16 v[54:57], v[174:177], v[186:189], v[110:113]
	v_mfma_f32_16x16x32_bf16 v[110:113], v[178:181], v[202:205], v[54:57]
	v_mfma_f32_16x16x32_bf16 v[54:57], v[166:169], v[182:185], v[98:101]
	v_mfma_f32_16x16x32_bf16 v[98:101], v[170:173], v[198:201], v[54:57]
	v_mfma_f32_16x16x32_bf16 v[54:57], v[174:177], v[182:185], v[94:97]
	v_mfma_f32_16x16x32_bf16 v[94:97], v[178:181], v[198:201], v[54:57]
	s_setprio 0
	s_setprio 1
	v_mfma_f32_16x16x32_bf16 v[54:57], v[150:153], v[194:197], v[138:141]
	v_mfma_f32_16x16x32_bf16 v[138:141], v[154:157], v[210:213], v[54:57]
	v_mfma_f32_16x16x32_bf16 v[54:57], v[158:161], v[194:197], v[134:137]
	v_mfma_f32_16x16x32_bf16 v[134:137], v[162:165], v[210:213], v[54:57]
	v_mfma_f32_16x16x32_bf16 v[54:57], v[150:153], v[190:193], v[122:125]
	v_mfma_f32_16x16x32_bf16 v[122:125], v[154:157], v[206:209], v[54:57]
	v_mfma_f32_16x16x32_bf16 v[54:57], v[158:161], v[190:193], v[118:121]
	v_mfma_f32_16x16x32_bf16 v[118:121], v[162:165], v[206:209], v[54:57]
	s_setprio 0
	s_setprio 1
	v_mfma_f32_16x16x32_bf16 v[54:57], v[150:153], v[186:189], v[106:109]
	v_mfma_f32_16x16x32_bf16 v[106:109], v[154:157], v[202:205], v[54:57]
	v_mfma_f32_16x16x32_bf16 v[54:57], v[158:161], v[186:189], v[102:105]
	v_mfma_f32_16x16x32_bf16 v[102:105], v[162:165], v[202:205], v[54:57]
	v_mfma_f32_16x16x32_bf16 v[54:57], v[150:153], v[182:185], v[90:93]
	v_mfma_f32_16x16x32_bf16 v[90:93], v[154:157], v[198:201], v[54:57]
	v_mfma_f32_16x16x32_bf16 v[54:57], v[158:161], v[182:185], v[86:89]
	v_mfma_f32_16x16x32_bf16 v[86:89], v[162:165], v[198:201], v[54:57]
	s_setprio 0
	s_barrier
	s_and_b64 vcc, exec, s[0:1]
	s_cbranch_vccnz .LBB0_1562
	ds_read_b128 v[194:197], v248 offset:49152
	ds_read_b128 v[210:213], v248 offset:50176
	ds_read_b128 v[190:193], v248 offset:51200
	ds_read_b128 v[206:209], v248 offset:52224
	ds_read_b128 v[186:189], v248 offset:53248
	ds_read_b128 v[202:205], v248 offset:54272
	ds_read_b128 v[182:185], v248 offset:55296
	ds_read_b128 v[198:201], v248 offset:56320
.LBB0_1562:
	s_mov_b32 m0, s56
	s_nop 1
	v_lshl_add_u64 v[54:55], v[226:227], 0, s[66:67]
	s_add_u32 s42, s42, 0x40080
	global_load_lds_dwordx4 v[54:55], off
	v_lshl_add_u64 v[54:55], v[228:229], 0, s[66:67]
	s_mov_b32 m0, s57
	s_addc_u32 s43, s43, 0
	global_load_lds_dwordx4 v[54:55], off
	v_lshl_add_u64 v[54:55], s[42:43], 0, v[0:1]
	s_mov_b32 m0, s60
	s_and_b64 vcc, exec, s[0:1]
	global_load_lds_dwordx4 v[54:55], off
	v_lshl_add_u64 v[54:55], s[42:43], 0, v[220:221]
	s_mov_b32 m0, s61
	s_nop 0
	global_load_lds_dwordx4 v[54:55], off
	v_lshl_add_u64 v[54:55], v[230:231], 0, s[66:67]
	s_mov_b32 m0, s58
	s_nop 0
	global_load_lds_dwordx4 v[54:55], off
	v_lshl_add_u64 v[54:55], v[232:233], 0, s[66:67]
	s_mov_b32 m0, s59
	s_nop 0
	global_load_lds_dwordx4 v[54:55], off
	s_waitcnt vmcnt(8)
	s_waitcnt lgkmcnt(0)
	s_barrier
	s_cbranch_vccnz .LBB0_1555
	s_setprio 1
	s_waitcnt lgkmcnt(0)
	v_mfma_f32_16x16x32_bf16 v[54:57], v[166:169], v[194:197], v[82:85]
	v_mfma_f32_16x16x32_bf16 v[82:85], v[170:173], v[210:213], v[54:57]
	v_mfma_f32_16x16x32_bf16 v[54:57], v[174:177], v[194:197], v[78:81]
	v_mfma_f32_16x16x32_bf16 v[50:53], v[166:169], v[190:193], v[50:53]
	v_mfma_f32_16x16x32_bf16 v[46:49], v[174:177], v[190:193], v[46:49]
	v_mfma_f32_16x16x32_bf16 v[34:37], v[166:169], v[186:189], v[34:37]
	v_mfma_f32_16x16x32_bf16 v[30:33], v[174:177], v[186:189], v[30:33]
	v_mfma_f32_16x16x32_bf16 v[18:21], v[166:169], v[182:185], v[18:21]
	s_setprio 0
	s_setprio 1
	v_mfma_f32_16x16x32_bf16 v[14:17], v[174:177], v[182:185], v[14:17]
	v_mfma_f32_16x16x32_bf16 v[78:81], v[178:181], v[210:213], v[54:57]
	v_mfma_f32_16x16x32_bf16 v[50:53], v[170:173], v[206:209], v[50:53]
	v_mfma_f32_16x16x32_bf16 v[46:49], v[178:181], v[206:209], v[46:49]
	v_mfma_f32_16x16x32_bf16 v[34:37], v[170:173], v[202:205], v[34:37]
	v_mfma_f32_16x16x32_bf16 v[30:33], v[178:181], v[202:205], v[30:33]
	v_mfma_f32_16x16x32_bf16 v[18:21], v[170:173], v[198:201], v[18:21]
	v_mfma_f32_16x16x32_bf16 v[14:17], v[178:181], v[198:201], v[14:17]
	s_setprio 0
	s_setprio 1
	v_mfma_f32_16x16x32_bf16 v[54:57], v[150:153], v[194:197], v[70:73]
	v_mfma_f32_16x16x32_bf16 v[70:73], v[154:157], v[210:213], v[54:57]
	v_mfma_f32_16x16x32_bf16 v[54:57], v[158:161], v[194:197], v[62:65]
	v_mfma_f32_16x16x32_bf16 v[42:45], v[150:153], v[190:193], v[42:45]
	v_mfma_f32_16x16x32_bf16 v[38:41], v[158:161], v[190:193], v[38:41]
	v_mfma_f32_16x16x32_bf16 v[26:29], v[150:153], v[186:189], v[26:29]
	v_mfma_f32_16x16x32_bf16 v[22:25], v[158:161], v[186:189], v[22:25]
	v_mfma_f32_16x16x32_bf16 v[10:13], v[150:153], v[182:185], v[10:13]
	s_setprio 0
	s_setprio 1
	v_mfma_f32_16x16x32_bf16 v[6:9], v[158:161], v[182:185], v[6:9]
	v_mfma_f32_16x16x32_bf16 v[62:65], v[162:165], v[210:213], v[54:57]
	v_mfma_f32_16x16x32_bf16 v[42:45], v[154:157], v[206:209], v[42:45]
	v_mfma_f32_16x16x32_bf16 v[38:41], v[162:165], v[206:209], v[38:41]
	v_mfma_f32_16x16x32_bf16 v[26:29], v[154:157], v[202:205], v[26:29]
	v_mfma_f32_16x16x32_bf16 v[22:25], v[162:165], v[202:205], v[22:25]
	v_mfma_f32_16x16x32_bf16 v[10:13], v[154:157], v[198:201], v[10:13]
	v_mfma_f32_16x16x32_bf16 v[6:9], v[162:165], v[198:201], v[6:9]
	s_setprio 0
	s_branch .LBB0_1555

.Lrw_done_g1_0:
	s_waitcnt lgkmcnt(0)
	v_mov_b32_e32 v169, v1
	s_barrier
	s_setprio 1
	s_waitcnt lgkmcnt(0)
	v_mfma_scale_f32_16x16x128_f8f6f4 v[150:153], v[26:33], v[198:205], 0, v234, v235 op_sel_hi:[0,0,0]
	v_mfma_scale_f32_16x16x128_f8f6f4 v[146:149], v[18:25], v[198:205], 0, v234, v235 op_sel_hi:[0,0,0]
	v_mfma_scale_f32_16x16x128_f8f6f4 v[142:145], v[26:33], v[206:213], 0, v234, v235 op_sel_hi:[0,0,0]
	v_mfma_scale_f32_16x16x128_f8f6f4 v[138:141], v[18:25], v[206:213], 0, v234, v235 op_sel_hi:[0,0,0]
	s_setprio 0
	s_setprio 1
	v_mfma_scale_f32_16x16x128_f8f6f4 v[134:137], v[26:33], v[216:223], 0, v234, v235 op_sel_hi:[0,0,0]
	v_mfma_scale_f32_16x16x128_f8f6f4 v[130:133], v[18:25], v[216:223], 0, v234, v235 op_sel_hi:[0,0,0]
	v_mfma_scale_f32_16x16x128_f8f6f4 v[126:129], v[26:33], v[224:231], 0, v234, v235 op_sel_hi:[0,0,0]
	v_mfma_scale_f32_16x16x128_f8f6f4 v[122:125], v[18:25], v[224:231], 0, v234, v235 op_sel_hi:[0,0,0]
	s_setprio 0
	s_setprio 1
	v_mfma_scale_f32_16x16x128_f8f6f4 v[118:121], v[10:17], v[198:205], 0, v234, v235 op_sel_hi:[0,0,0]
	v_mfma_scale_f32_16x16x128_f8f6f4 v[114:117], v[2:9], v[198:205], 0, v234, v235 op_sel_hi:[0,0,0]
	v_mfma_scale_f32_16x16x128_f8f6f4 v[110:113], v[10:17], v[206:213], 0, v234, v235 op_sel_hi:[0,0,0]
	v_mfma_scale_f32_16x16x128_f8f6f4 v[106:109], v[2:9], v[206:213], 0, v234, v235 op_sel_hi:[0,0,0]
	s_setprio 0
	s_setprio 1
	v_mfma_scale_f32_16x16x128_f8f6f4 v[102:105], v[10:17], v[216:223], 0, v234, v235 op_sel_hi:[0,0,0]
	v_mfma_scale_f32_16x16x128_f8f6f4 v[98:101], v[2:9], v[216:223], 0, v234, v235 op_sel_hi:[0,0,0]
	v_mfma_scale_f32_16x16x128_f8f6f4 v[94:97], v[10:17], v[224:231], 0, v234, v235 op_sel_hi:[0,0,0]
	v_mfma_scale_f32_16x16x128_f8f6f4 v[90:93], v[2:9], v[224:231], 0, v234, v235 op_sel_hi:[0,0,0]
	s_setprio 0
	s_barrier
	v_lshl_add_u64 v[170:171], s[4:5], 0, v[162:163]
	s_mov_b64 s[54:55], 0x100
	s_mov_b32 m0, s68
	v_lshl_add_u64 v[172:173], v[170:171], 0, s[54:55]
	ds_read_b128 v[198:201], v192 offset:16384
	ds_read_b128 v[202:205], v192 offset:17408
	ds_read_b128 v[206:209], v192 offset:18432
	ds_read_b128 v[210:213], v192 offset:19456
	ds_read_b128 v[216:219], v192 offset:20480
	ds_read_b128 v[220:223], v192 offset:21504
	ds_read_b128 v[224:227], v192 offset:22528
	ds_read_b128 v[228:231], v192 offset:23552
	global_load_lds_dwordx4 v[172:173], off
	v_lshl_add_u64 v[172:173], s[4:5], 0, v[164:165]
	v_lshl_add_u64 v[232:233], v[172:173], 0, s[54:55]
	s_add_u32 s54, s4, 0x20100
	s_mov_b32 m0, s60
	s_addc_u32 s55, s5, 0
	global_load_lds_dwordx4 v[232:233], off
	v_lshl_add_u64 v[232:233], s[54:55], 0, v[162:163]
	s_mov_b32 m0, s61
	v_lshlrev_b32_e32 v0, 10, v195
	global_load_lds_dwordx4 v[232:233], off
	v_lshl_add_u64 v[232:233], s[54:55], 0, v[164:165]
	s_mov_b32 m0, s62
	v_and_or_b32 v0, v0, s82, v174
	global_load_lds_dwordx4 v[232:233], off
	v_bfe_u32 v197, v195, 16, 16
	s_mov_b32 m0, s65
	v_lshl_add_u32 v197, v197, 10, v175
	global_load_lds_dwordx4 v0, s[34:35]
	s_mov_b32 m0, s63
	s_nop 0
	global_load_lds_dwordx4 v197, s[34:35]
	s_cmp_eq_u32 s23, 0
	s_cbranch_scc1 .Lrw_first_g1_1
	s_waitcnt vmcnt(12)
	s_branch .Lrw_done_g1_1

.Lrw_done_g1_1:
	s_waitcnt lgkmcnt(0)
	s_barrier
	s_setprio 1
	s_waitcnt lgkmcnt(0)
	v_mfma_scale_f32_16x16x128_f8f6f4 v[86:89], v[26:33], v[198:205], 0, v234, v235 op_sel_hi:[0,0,0]
	v_mfma_scale_f32_16x16x128_f8f6f4 v[82:85], v[18:25], v[198:205], 0, v234, v235 op_sel_hi:[0,0,0]
	v_mfma_scale_f32_16x16x128_f8f6f4 v[78:81], v[26:33], v[206:213], 0, v234, v235 op_sel_hi:[0,0,0]
	v_mfma_scale_f32_16x16x128_f8f6f4 v[74:77], v[18:25], v[206:213], 0, v234, v235 op_sel_hi:[0,0,0]
	s_setprio 0
	s_setprio 1
	v_mfma_scale_f32_16x16x128_f8f6f4 v[70:73], v[26:33], v[216:223], 0, v234, v235 op_sel_hi:[0,0,0]
	v_mfma_scale_f32_16x16x128_f8f6f4 v[66:69], v[18:25], v[216:223], 0, v234, v235 op_sel_hi:[0,0,0]
	v_mfma_scale_f32_16x16x128_f8f6f4 v[62:65], v[26:33], v[224:231], 0, v234, v235 op_sel_hi:[0,0,0]
	v_mfma_scale_f32_16x16x128_f8f6f4 v[58:61], v[18:25], v[224:231], 0, v234, v235 op_sel_hi:[0,0,0]
	s_setprio 0
	s_setprio 1
	v_mfma_scale_f32_16x16x128_f8f6f4 v[54:57], v[10:17], v[198:205], 0, v234, v235 op_sel_hi:[0,0,0]
	v_mfma_scale_f32_16x16x128_f8f6f4 v[50:53], v[2:9], v[198:205], 0, v234, v235 op_sel_hi:[0,0,0]
	v_mfma_scale_f32_16x16x128_f8f6f4 v[46:49], v[10:17], v[206:213], 0, v234, v235 op_sel_hi:[0,0,0]
	v_mfma_scale_f32_16x16x128_f8f6f4 v[42:45], v[2:9], v[206:213], 0, v234, v235 op_sel_hi:[0,0,0]
	s_setprio 0
	s_setprio 1
	v_mfma_scale_f32_16x16x128_f8f6f4 v[38:41], v[10:17], v[216:223], 0, v234, v235 op_sel_hi:[0,0,0]
	v_mfma_scale_f32_16x16x128_f8f6f4 v[34:37], v[2:9], v[216:223], 0, v234, v235 op_sel_hi:[0,0,0]
	v_mfma_scale_f32_16x16x128_f8f6f4 v[154:157], v[10:17], v[224:231], 0, v234, v235 op_sel_hi:[0,0,0]
	v_mfma_scale_f32_16x16x128_f8f6f4 v[158:161], v[2:9], v[224:231], 0, v234, v235 op_sel_hi:[0,0,0]
	s_setprio 0
	s_barrier
	ds_read_b128 v[18:21], v184
	ds_read_b128 v[22:25], v185
	ds_read_b128 v[26:29], v186
	ds_read_b128 v[30:33], v187
	ds_read_b128 v[2:5], v188
	ds_read_b128 v[6:9], v189
	ds_read_b128 v[10:13], v190
	ds_read_b128 v[14:17], v191
	s_mov_b32 m0, s10
	ds_read_b128 v[198:201], v192 offset:32768
	ds_read_b128 v[202:205], v192 offset:33792
	ds_read_b128 v[206:209], v192 offset:34816
	ds_read_b128 v[210:213], v192 offset:35840
	ds_read_b128 v[216:219], v192 offset:36864
	ds_read_b128 v[220:223], v192 offset:37888
	ds_read_b128 v[224:227], v192 offset:38912
	ds_read_b128 v[228:231], v192 offset:39936
	global_load_lds_dwordx4 v166, s[34:35]
	s_mov_b32 m0, s11
	s_nop 0
	global_load_lds_dwordx4 v168, s[34:35]
	s_waitcnt vmcnt(8)
	s_waitcnt lgkmcnt(0)
	s_barrier
	s_setprio 1
	s_waitcnt lgkmcnt(0)
	v_mfma_scale_f32_16x16x128_f8f6f4 v[150:153], v[18:25], v[198:205], v[150:153], v234, v235 op_sel_hi:[0,0,0]
	v_mfma_scale_f32_16x16x128_f8f6f4 v[146:149], v[26:33], v[198:205], v[146:149], v234, v235 op_sel_hi:[0,0,0]
	v_mfma_scale_f32_16x16x128_f8f6f4 v[142:145], v[18:25], v[206:213], v[142:145], v234, v235 op_sel_hi:[0,0,0]
	v_mfma_scale_f32_16x16x128_f8f6f4 v[138:141], v[26:33], v[206:213], v[138:141], v234, v235 op_sel_hi:[0,0,0]
	s_setprio 0
	s_setprio 1
	v_mfma_scale_f32_16x16x128_f8f6f4 v[134:137], v[18:25], v[216:223], v[134:137], v234, v235 op_sel_hi:[0,0,0]
	v_mfma_scale_f32_16x16x128_f8f6f4 v[130:133], v[26:33], v[216:223], v[130:133], v234, v235 op_sel_hi:[0,0,0]
	v_mfma_scale_f32_16x16x128_f8f6f4 v[126:129], v[18:25], v[224:231], v[126:129], v234, v235 op_sel_hi:[0,0,0]
	v_mfma_scale_f32_16x16x128_f8f6f4 v[122:125], v[26:33], v[224:231], v[122:125], v234, v235 op_sel_hi:[0,0,0]
	s_setprio 0
	s_setprio 1
	v_mfma_scale_f32_16x16x128_f8f6f4 v[118:121], v[2:9], v[198:205], v[118:121], v234, v235 op_sel_hi:[0,0,0]
	v_mfma_scale_f32_16x16x128_f8f6f4 v[114:117], v[10:17], v[198:205], v[114:117], v234, v235 op_sel_hi:[0,0,0]
	v_mfma_scale_f32_16x16x128_f8f6f4 v[110:113], v[2:9], v[206:213], v[110:113], v234, v235 op_sel_hi:[0,0,0]
	v_mfma_scale_f32_16x16x128_f8f6f4 v[106:109], v[10:17], v[206:213], v[106:109], v234, v235 op_sel_hi:[0,0,0]
	s_setprio 0
	s_setprio 1
	v_mfma_scale_f32_16x16x128_f8f6f4 v[102:105], v[2:9], v[216:223], v[102:105], v234, v235 op_sel_hi:[0,0,0]
	v_mfma_scale_f32_16x16x128_f8f6f4 v[98:101], v[10:17], v[216:223], v[98:101], v234, v235 op_sel_hi:[0,0,0]
	v_mfma_scale_f32_16x16x128_f8f6f4 v[94:97], v[2:9], v[224:231], v[94:97], v234, v235 op_sel_hi:[0,0,0]
	v_mfma_scale_f32_16x16x128_f8f6f4 v[90:93], v[10:17], v[224:231], v[90:93], v234, v235 op_sel_hi:[0,0,0]
	s_setprio 0
	s_barrier
	s_mov_b64 s[54:55], 0x180
	s_mov_b32 m0, s64
	v_lshl_add_u64 v[170:171], v[170:171], 0, s[54:55]
	ds_read_b128 v[198:201], v192 offset:49152
	ds_read_b128 v[202:205], v192 offset:50176
	ds_read_b128 v[206:209], v192 offset:51200
	ds_read_b128 v[210:213], v192 offset:52224
	ds_read_b128 v[216:219], v192 offset:53248
	ds_read_b128 v[220:223], v192 offset:54272
	ds_read_b128 v[224:227], v192 offset:55296
	ds_read_b128 v[228:231], v192 offset:56320
	global_load_lds_dwordx4 v[170:171], off
	v_lshl_add_u64 v[170:171], v[172:173], 0, s[54:55]
	s_add_u32 s54, s4, 0x20180
	s_mov_b32 m0, s81
	s_addc_u32 s55, s5, 0
	global_load_lds_dwordx4 v[170:171], off
	v_lshl_add_u64 v[170:171], s[54:55], 0, v[162:163]
	s_mov_b32 m0, s49
	s_nop 0
	global_load_lds_dwordx4 v[170:171], off
	v_lshl_add_u64 v[170:171], s[54:55], 0, v[164:165]
	s_mov_b32 m0, s30
	s_nop 0
	global_load_lds_dwordx4 v[170:171], off
	s_mov_b32 m0, s6
	s_nop 0
	global_load_lds_dwordx4 v0, s[36:37]
	s_mov_b32 m0, s7
	s_nop 0
	global_load_lds_dwordx4 v197, s[36:37]
	s_waitcnt vmcnt(8)
	s_waitcnt lgkmcnt(0)
	s_barrier
	s_setprio 1
	s_waitcnt lgkmcnt(0)
	v_mfma_scale_f32_16x16x128_f8f6f4 v[86:89], v[18:25], v[198:205], v[86:89], v234, v235 op_sel_hi:[0,0,0]
	v_mfma_scale_f32_16x16x128_f8f6f4 v[82:85], v[26:33], v[198:205], v[82:85], v234, v235 op_sel_hi:[0,0,0]
	v_mfma_scale_f32_16x16x128_f8f6f4 v[78:81], v[18:25], v[206:213], v[78:81], v234, v235 op_sel_hi:[0,0,0]
	v_mfma_scale_f32_16x16x128_f8f6f4 v[74:77], v[26:33], v[206:213], v[74:77], v234, v235 op_sel_hi:[0,0,0]
	s_setprio 0
	s_setprio 1
	v_mfma_scale_f32_16x16x128_f8f6f4 v[70:73], v[18:25], v[216:223], v[70:73], v234, v235 op_sel_hi:[0,0,0]
	v_mfma_scale_f32_16x16x128_f8f6f4 v[66:69], v[26:33], v[216:223], v[66:69], v234, v235 op_sel_hi:[0,0,0]
	v_mfma_scale_f32_16x16x128_f8f6f4 v[62:65], v[18:25], v[224:231], v[62:65], v234, v235 op_sel_hi:[0,0,0]
	v_mfma_scale_f32_16x16x128_f8f6f4 v[58:61], v[26:33], v[224:231], v[58:61], v234, v235 op_sel_hi:[0,0,0]
	s_setprio 0
	s_setprio 1
	v_mfma_scale_f32_16x16x128_f8f6f4 v[54:57], v[2:9], v[198:205], v[54:57], v234, v235 op_sel_hi:[0,0,0]
	v_mfma_scale_f32_16x16x128_f8f6f4 v[50:53], v[10:17], v[198:205], v[50:53], v234, v235 op_sel_hi:[0,0,0]
	v_mfma_scale_f32_16x16x128_f8f6f4 v[46:49], v[2:9], v[206:213], v[46:49], v234, v235 op_sel_hi:[0,0,0]
	v_mfma_scale_f32_16x16x128_f8f6f4 v[42:45], v[10:17], v[206:213], v[42:45], v234, v235 op_sel_hi:[0,0,0]
	s_setprio 0
	s_setprio 1
	v_mfma_scale_f32_16x16x128_f8f6f4 v[38:41], v[2:9], v[216:223], v[38:41], v234, v235 op_sel_hi:[0,0,0]
	v_mfma_scale_f32_16x16x128_f8f6f4 v[34:37], v[10:17], v[216:223], v[34:37], v234, v235 op_sel_hi:[0,0,0]
	v_mfma_scale_f32_16x16x128_f8f6f4 v[154:157], v[2:9], v[224:231], v[154:157], v234, v235 op_sel_hi:[0,0,0]
	v_mfma_scale_f32_16x16x128_f8f6f4 v[158:161], v[10:17], v[224:231], v[158:161], v234, v235 op_sel_hi:[0,0,0]
	s_setprio 0
	s_barrier
	s_add_u32 s43, s4, 0x200
	s_addc_u32 s45, s5, 0
	s_mov_b32 s74, 0
	s_mov_b64 s[54:55], s[36:37]
	s_branch .LBB0_2003
.LBB0_2002:
	ds_read_b128 v[2:5], v183
	ds_read_b128 v[6:9], v182
	ds_read_b128 v[10:13], v181
	ds_read_b128 v[14:17], v180
	ds_read_b128 v[26:29], v179
	ds_read_b128 v[30:33], v178
	ds_read_b128 v[198:201], v177
	ds_read_b128 v[202:205], v176
	s_add_u32 s58, s54, 0x80
	s_addc_u32 s59, s55, 0
	s_and_b64 s[56:57], s[4:5], exec
	s_cselect_b32 s59, s9, s59
	s_cselect_b32 s58, s8, s58
	s_cselect_b32 s57, s47, s45
	s_cselect_b32 s56, s46, s43
	s_mov_b32 m0, s27
	v_lshl_add_u64 v[170:171], s[54:55], 0, v[166:167]
	ds_read_b128 v[18:21], v192
	ds_read_b128 v[22:25], v192 offset:1024
	ds_read_b128 v[206:209], v192 offset:2048
	ds_read_b128 v[210:213], v192 offset:3072
	ds_read_b128 v[216:219], v192 offset:4096
	ds_read_b128 v[220:223], v192 offset:5120
	ds_read_b128 v[224:227], v192 offset:6144
	ds_read_b128 v[228:231], v192 offset:7168
	global_load_lds_dwordx4 v[170:171], off
	v_lshl_add_u64 v[170:171], s[54:55], 0, v[168:169]
	s_mov_b32 m0, s41
	s_nop 0
	global_load_lds_dwordx4 v[170:171], off
	s_waitcnt vmcnt(8)
	s_waitcnt lgkmcnt(0)
	s_barrier
	s_setprio 1
	s_waitcnt lgkmcnt(0)
	v_mfma_scale_f32_16x16x128_f8f6f4 v[150:153], v[2:9], v[18:25], v[150:153], v234, v235 op_sel_hi:[0,0,0]
	v_mfma_scale_f32_16x16x128_f8f6f4 v[146:149], v[10:17], v[18:25], v[146:149], v234, v235 op_sel_hi:[0,0,0]
	v_mfma_scale_f32_16x16x128_f8f6f4 v[142:145], v[2:9], v[206:213], v[142:145], v234, v235 op_sel_hi:[0,0,0]
	v_mfma_scale_f32_16x16x128_f8f6f4 v[138:141], v[10:17], v[206:213], v[138:141], v234, v235 op_sel_hi:[0,0,0]
	s_setprio 0
	s_setprio 1
	v_mfma_scale_f32_16x16x128_f8f6f4 v[134:137], v[2:9], v[216:223], v[134:137], v234, v235 op_sel_hi:[0,0,0]
	v_mfma_scale_f32_16x16x128_f8f6f4 v[130:133], v[10:17], v[216:223], v[130:133], v234, v235 op_sel_hi:[0,0,0]
	v_mfma_scale_f32_16x16x128_f8f6f4 v[126:129], v[2:9], v[224:231], v[126:129], v234, v235 op_sel_hi:[0,0,0]
	v_mfma_scale_f32_16x16x128_f8f6f4 v[122:125], v[10:17], v[224:231], v[122:125], v234, v235 op_sel_hi:[0,0,0]
	s_setprio 0
	s_setprio 1
	v_mfma_scale_f32_16x16x128_f8f6f4 v[118:121], v[26:33], v[18:25], v[118:121], v234, v235 op_sel_hi:[0,0,0]
	v_mfma_scale_f32_16x16x128_f8f6f4 v[114:117], v[198:205], v[18:25], v[114:117], v234, v235 op_sel_hi:[0,0,0]
	v_mfma_scale_f32_16x16x128_f8f6f4 v[110:113], v[26:33], v[206:213], v[110:113], v234, v235 op_sel_hi:[0,0,0]
	v_mfma_scale_f32_16x16x128_f8f6f4 v[106:109], v[198:205], v[206:213], v[106:109], v234, v235 op_sel_hi:[0,0,0]
	s_setprio 0
	s_setprio 1
	v_mfma_scale_f32_16x16x128_f8f6f4 v[102:105], v[26:33], v[216:223], v[102:105], v234, v235 op_sel_hi:[0,0,0]
	v_mfma_scale_f32_16x16x128_f8f6f4 v[98:101], v[198:205], v[216:223], v[98:101], v234, v235 op_sel_hi:[0,0,0]
	v_mfma_scale_f32_16x16x128_f8f6f4 v[94:97], v[26:33], v[224:231], v[94:97], v234, v235 op_sel_hi:[0,0,0]
	v_mfma_scale_f32_16x16x128_f8f6f4 v[90:93], v[198:205], v[224:231], v[90:93], v234, v235 op_sel_hi:[0,0,0]
	s_setprio 0
	s_barrier
	s_mov_b32 m0, s68
	v_lshl_add_u64 v[18:19], s[56:57], 0, v[162:163]
	s_add_u32 vcc_lo, s56, 0x20000
	ds_read_b128 v[206:209], v192 offset:16384
	ds_read_b128 v[210:213], v192 offset:17408
	ds_read_b128 v[216:219], v192 offset:18432
	ds_read_b128 v[220:223], v192 offset:19456
	ds_read_b128 v[224:227], v192 offset:20480
	ds_read_b128 v[228:231], v192 offset:21504
	ds_read_b128 v[244:247], v192 offset:22528
	ds_read_b128 v[248:251], v192 offset:23552
	global_load_lds_dwordx4 v[18:19], off
	v_lshl_add_u64 v[20:21], s[56:57], 0, v[164:165]
	s_mov_b32 m0, s60
	s_addc_u32 vcc_hi, s57, 0
	global_load_lds_dwordx4 v[20:21], off
	v_lshl_add_u64 v[22:23], vcc, 0, v[162:163]
	s_mov_b32 m0, s61
	s_nop 0
	global_load_lds_dwordx4 v[22:23], off
	v_lshl_add_u64 v[22:23], vcc, 0, v[164:165]
	s_mov_b32 m0, s62
	s_nop 0
	global_load_lds_dwordx4 v[22:23], off
	v_cndmask_b32_e64 v22, v195, v193, s[4:5]
	v_lshlrev_b32_e32 v0, 10, v22
	v_and_or_b32 v0, v0, s82, v174
	v_bfe_u32 v22, v22, 16, 16
	s_mov_b32 m0, s65
	v_lshl_add_u32 v22, v22, 10, v175
	global_load_lds_dwordx4 v0, s[58:59]
	s_mov_b32 m0, s63
	v_mov_b32_e32 v23, v1
	global_load_lds_dwordx4 v22, s[58:59]
	s_waitcnt vmcnt(8)
	s_waitcnt lgkmcnt(0)
	v_lshl_add_u64 v[24:25], s[58:59], 0, v[0:1]
	v_lshl_add_u64 v[22:23], s[58:59], 0, v[22:23]
	s_barrier
	s_setprio 1
	s_waitcnt lgkmcnt(0)
	v_mfma_scale_f32_16x16x128_f8f6f4 v[86:89], v[2:9], v[206:213], v[86:89], v234, v235 op_sel_hi:[0,0,0]
	v_mfma_scale_f32_16x16x128_f8f6f4 v[82:85], v[10:17], v[206:213], v[82:85], v234, v235 op_sel_hi:[0,0,0]
	v_mfma_scale_f32_16x16x128_f8f6f4 v[78:81], v[2:9], v[216:223], v[78:81], v234, v235 op_sel_hi:[0,0,0]
	v_mfma_scale_f32_16x16x128_f8f6f4 v[74:77], v[10:17], v[216:223], v[74:77], v234, v235 op_sel_hi:[0,0,0]
	s_setprio 0
	s_setprio 1
	v_mfma_scale_f32_16x16x128_f8f6f4 v[70:73], v[2:9], v[224:231], v[70:73], v234, v235 op_sel_hi:[0,0,0]
	v_mfma_scale_f32_16x16x128_f8f6f4 v[66:69], v[10:17], v[224:231], v[66:69], v234, v235 op_sel_hi:[0,0,0]
	v_mfma_scale_f32_16x16x128_f8f6f4 v[62:65], v[2:9], v[244:251], v[62:65], v234, v235 op_sel_hi:[0,0,0]
	v_mfma_scale_f32_16x16x128_f8f6f4 v[58:61], v[10:17], v[244:251], v[58:61], v234, v235 op_sel_hi:[0,0,0]
	s_setprio 0
	s_setprio 1
	v_mfma_scale_f32_16x16x128_f8f6f4 v[54:57], v[26:33], v[206:213], v[54:57], v234, v235 op_sel_hi:[0,0,0]
	v_mfma_scale_f32_16x16x128_f8f6f4 v[50:53], v[198:205], v[206:213], v[50:53], v234, v235 op_sel_hi:[0,0,0]
	v_mfma_scale_f32_16x16x128_f8f6f4 v[46:49], v[26:33], v[216:223], v[46:49], v234, v235 op_sel_hi:[0,0,0]
	v_mfma_scale_f32_16x16x128_f8f6f4 v[42:45], v[198:205], v[216:223], v[42:45], v234, v235 op_sel_hi:[0,0,0]
	s_setprio 0
	s_setprio 1
	v_mfma_scale_f32_16x16x128_f8f6f4 v[38:41], v[26:33], v[224:231], v[38:41], v234, v235 op_sel_hi:[0,0,0]
	v_mfma_scale_f32_16x16x128_f8f6f4 v[34:37], v[198:205], v[224:231], v[34:37], v234, v235 op_sel_hi:[0,0,0]
	v_mfma_scale_f32_16x16x128_f8f6f4 v[154:157], v[26:33], v[244:251], v[154:157], v234, v235 op_sel_hi:[0,0,0]
	v_mfma_scale_f32_16x16x128_f8f6f4 v[158:161], v[198:205], v[244:251], v[158:161], v234, v235 op_sel_hi:[0,0,0]
	s_setprio 0
	s_barrier
	ds_read_b128 v[10:13], v184
	ds_read_b128 v[14:17], v185
	ds_read_b128 v[26:29], v186
	ds_read_b128 v[30:33], v187
	ds_read_b128 v[2:5], v188
	ds_read_b128 v[6:9], v189
	ds_read_b128 v[198:201], v190
	ds_read_b128 v[202:205], v191
	v_cndmask_b32_e64 v0, v196, v194, s[4:5]
	v_lshlrev_b32_e32 v170, 10, v0
	s_mov_b32 m0, s10
	v_and_or_b32 v170, v170, s82, v174
	v_bfe_u32 v0, v0, 16, 16
	ds_read_b128 v[206:209], v192 offset:32768
	ds_read_b128 v[210:213], v192 offset:33792
	ds_read_b128 v[216:219], v192 offset:34816
	ds_read_b128 v[220:223], v192 offset:35840
	ds_read_b128 v[224:227], v192 offset:36864
	ds_read_b128 v[228:231], v192 offset:37888
	ds_read_b128 v[244:247], v192 offset:38912
	ds_read_b128 v[248:251], v192 offset:39936
	v_lshl_add_u32 v0, v0, 10, v175
	global_load_lds_dwordx4 v170, s[58:59]
	s_mov_b32 m0, s11
	s_nop 0
	global_load_lds_dwordx4 v0, s[58:59]
	s_waitcnt vmcnt(8)
	s_waitcnt lgkmcnt(0)
	s_barrier
	s_setprio 1
	s_waitcnt lgkmcnt(0)
	v_mfma_scale_f32_16x16x128_f8f6f4 v[150:153], v[10:17], v[206:213], v[150:153], v234, v235 op_sel_hi:[0,0,0]
	v_mfma_scale_f32_16x16x128_f8f6f4 v[146:149], v[26:33], v[206:213], v[146:149], v234, v235 op_sel_hi:[0,0,0]
	v_mfma_scale_f32_16x16x128_f8f6f4 v[142:145], v[10:17], v[216:223], v[142:145], v234, v235 op_sel_hi:[0,0,0]
	v_mfma_scale_f32_16x16x128_f8f6f4 v[138:141], v[26:33], v[216:223], v[138:141], v234, v235 op_sel_hi:[0,0,0]
	s_setprio 0
	s_setprio 1
	v_mfma_scale_f32_16x16x128_f8f6f4 v[134:137], v[10:17], v[224:231], v[134:137], v234, v235 op_sel_hi:[0,0,0]
	v_mfma_scale_f32_16x16x128_f8f6f4 v[130:133], v[26:33], v[224:231], v[130:133], v234, v235 op_sel_hi:[0,0,0]
	v_mfma_scale_f32_16x16x128_f8f6f4 v[126:129], v[10:17], v[244:251], v[126:129], v234, v235 op_sel_hi:[0,0,0]
	v_mfma_scale_f32_16x16x128_f8f6f4 v[122:125], v[26:33], v[244:251], v[122:125], v234, v235 op_sel_hi:[0,0,0]
	s_setprio 0
	s_setprio 1
	v_mfma_scale_f32_16x16x128_f8f6f4 v[118:121], v[2:9], v[206:213], v[118:121], v234, v235 op_sel_hi:[0,0,0]
	v_mfma_scale_f32_16x16x128_f8f6f4 v[114:117], v[198:205], v[206:213], v[114:117], v234, v235 op_sel_hi:[0,0,0]
	v_mfma_scale_f32_16x16x128_f8f6f4 v[110:113], v[2:9], v[216:223], v[110:113], v234, v235 op_sel_hi:[0,0,0]
	v_mfma_scale_f32_16x16x128_f8f6f4 v[106:109], v[198:205], v[216:223], v[106:109], v234, v235 op_sel_hi:[0,0,0]
	s_setprio 0
	s_setprio 1
	v_mfma_scale_f32_16x16x128_f8f6f4 v[102:105], v[2:9], v[224:231], v[102:105], v234, v235 op_sel_hi:[0,0,0]
	v_mfma_scale_f32_16x16x128_f8f6f4 v[98:101], v[198:205], v[224:231], v[98:101], v234, v235 op_sel_hi:[0,0,0]
	v_mfma_scale_f32_16x16x128_f8f6f4 v[94:97], v[2:9], v[244:251], v[94:97], v234, v235 op_sel_hi:[0,0,0]
	v_mfma_scale_f32_16x16x128_f8f6f4 v[90:93], v[198:205], v[244:251], v[90:93], v234, v235 op_sel_hi:[0,0,0]
	s_setprio 0
	s_barrier
	s_mov_b32 m0, s64
	v_lshl_add_u64 v[18:19], v[18:19], 0, s[66:67]
	s_add_u32 s4, s56, 0x20080
	ds_read_b128 v[206:209], v192 offset:49152
	ds_read_b128 v[210:213], v192 offset:50176
	ds_read_b128 v[216:219], v192 offset:51200
	ds_read_b128 v[220:223], v192 offset:52224
	ds_read_b128 v[224:227], v192 offset:53248
	ds_read_b128 v[228:231], v192 offset:54272
	ds_read_b128 v[244:247], v192 offset:55296
	ds_read_b128 v[248:251], v192 offset:56320
	global_load_lds_dwordx4 v[18:19], off
	v_lshl_add_u64 v[18:19], v[20:21], 0, s[66:67]
	s_mov_b32 m0, s81
	s_addc_u32 s5, s57, 0
	global_load_lds_dwordx4 v[18:19], off
	v_lshl_add_u64 v[18:19], s[4:5], 0, v[162:163]
	s_mov_b32 m0, s49
	s_nop 0
	global_load_lds_dwordx4 v[18:19], off
	v_lshl_add_u64 v[18:19], s[4:5], 0, v[164:165]
	s_mov_b32 m0, s30
	s_nop 0
	global_load_lds_dwordx4 v[18:19], off
	v_lshl_add_u64 v[18:19], v[24:25], 0, s[66:67]
	s_mov_b32 m0, s6
	s_nop 0
	global_load_lds_dwordx4 v[18:19], off
	v_lshl_add_u64 v[18:19], v[22:23], 0, s[66:67]
	s_mov_b32 m0, s7
	s_nop 0
	global_load_lds_dwordx4 v[18:19], off
	s_waitcnt vmcnt(8)
	s_waitcnt lgkmcnt(0)
	s_barrier
	s_setprio 1
	s_waitcnt lgkmcnt(0)
	v_mfma_scale_f32_16x16x128_f8f6f4 v[86:89], v[10:17], v[206:213], v[86:89], v234, v235 op_sel_hi:[0,0,0]
	v_mfma_scale_f32_16x16x128_f8f6f4 v[82:85], v[26:33], v[206:213], v[82:85], v234, v235 op_sel_hi:[0,0,0]
	v_mfma_scale_f32_16x16x128_f8f6f4 v[78:81], v[10:17], v[216:223], v[78:81], v234, v235 op_sel_hi:[0,0,0]
	v_mfma_scale_f32_16x16x128_f8f6f4 v[74:77], v[26:33], v[216:223], v[74:77], v234, v235 op_sel_hi:[0,0,0]
	s_setprio 0
	s_setprio 1
	v_mfma_scale_f32_16x16x128_f8f6f4 v[70:73], v[10:17], v[224:231], v[70:73], v234, v235 op_sel_hi:[0,0,0]
	v_mfma_scale_f32_16x16x128_f8f6f4 v[66:69], v[26:33], v[224:231], v[66:69], v234, v235 op_sel_hi:[0,0,0]
	v_mfma_scale_f32_16x16x128_f8f6f4 v[62:65], v[10:17], v[244:251], v[62:65], v234, v235 op_sel_hi:[0,0,0]
	v_mfma_scale_f32_16x16x128_f8f6f4 v[58:61], v[26:33], v[244:251], v[58:61], v234, v235 op_sel_hi:[0,0,0]
	s_setprio 0
	s_setprio 1
	v_mfma_scale_f32_16x16x128_f8f6f4 v[54:57], v[2:9], v[206:213], v[54:57], v234, v235 op_sel_hi:[0,0,0]
	v_mfma_scale_f32_16x16x128_f8f6f4 v[50:53], v[198:205], v[206:213], v[50:53], v234, v235 op_sel_hi:[0,0,0]
	v_mfma_scale_f32_16x16x128_f8f6f4 v[46:49], v[2:9], v[216:223], v[46:49], v234, v235 op_sel_hi:[0,0,0]
	v_mfma_scale_f32_16x16x128_f8f6f4 v[42:45], v[198:205], v[216:223], v[42:45], v234, v235 op_sel_hi:[0,0,0]
	s_setprio 0
	s_setprio 1
	v_mfma_scale_f32_16x16x128_f8f6f4 v[38:41], v[2:9], v[224:231], v[38:41], v234, v235 op_sel_hi:[0,0,0]
	v_mfma_scale_f32_16x16x128_f8f6f4 v[34:37], v[198:205], v[224:231], v[34:37], v234, v235 op_sel_hi:[0,0,0]
	v_mfma_scale_f32_16x16x128_f8f6f4 v[154:157], v[2:9], v[244:251], v[154:157], v234, v235 op_sel_hi:[0,0,0]
	v_mfma_scale_f32_16x16x128_f8f6f4 v[158:161], v[198:205], v[244:251], v[158:161], v234, v235 op_sel_hi:[0,0,0]
	s_setprio 0
	s_barrier
	s_add_i32 s74, s74, 2
	s_add_u32 s54, s54, 0x100
	s_addc_u32 s55, s55, 0
	s_add_u32 s43, s43, 0x100
	s_addc_u32 s45, s45, 0
	s_cmp_gt_u32 s74, 5
	s_cbranch_scc1 .LBB0_2005

.Lrw_done_g2_0:
	s_waitcnt lgkmcnt(0)
	s_barrier
	s_setprio 1
	s_waitcnt lgkmcnt(0)
	v_mfma_scale_f32_16x16x128_f8f6f4 v[158:161], v[18:25], v[172:179], 0, v234, v238 op_sel_hi:[0,0,0]
	v_mfma_scale_f32_16x16x128_f8f6f4 v[154:157], v[26:33], v[172:179], 0, v234, v238 op_sel_hi:[0,0,0]
	v_mfma_scale_f32_16x16x128_f8f6f4 v[150:153], v[18:25], v[198:205], 0, v234, v238 op_sel_hi:[0,0,0]
	v_mfma_scale_f32_16x16x128_f8f6f4 v[146:149], v[26:33], v[198:205], 0, v234, v238 op_sel_hi:[0,0,0]
	s_setprio 0
	s_setprio 1
	v_mfma_scale_f32_16x16x128_f8f6f4 v[142:145], v[18:25], v[206:213], 0, v234, v238 op_sel_hi:[0,0,0]
	v_mfma_scale_f32_16x16x128_f8f6f4 v[138:141], v[26:33], v[206:213], 0, v234, v238 op_sel_hi:[0,0,0]
	v_mfma_scale_f32_16x16x128_f8f6f4 v[134:137], v[18:25], v[216:223], 0, v234, v238 op_sel_hi:[0,0,0]
	v_mfma_scale_f32_16x16x128_f8f6f4 v[130:133], v[26:33], v[216:223], 0, v234, v238 op_sel_hi:[0,0,0]
	s_setprio 0
	s_setprio 1
	v_mfma_scale_f32_16x16x128_f8f6f4 v[126:129], v[2:9], v[172:179], 0, v234, v238 op_sel_hi:[0,0,0]
	v_mfma_scale_f32_16x16x128_f8f6f4 v[122:125], v[10:17], v[172:179], 0, v234, v238 op_sel_hi:[0,0,0]
	v_mfma_scale_f32_16x16x128_f8f6f4 v[118:121], v[2:9], v[198:205], 0, v234, v238 op_sel_hi:[0,0,0]
	v_mfma_scale_f32_16x16x128_f8f6f4 v[114:117], v[10:17], v[198:205], 0, v234, v238 op_sel_hi:[0,0,0]
	s_setprio 0
	s_setprio 1
	v_mfma_scale_f32_16x16x128_f8f6f4 v[110:113], v[2:9], v[206:213], 0, v234, v238 op_sel_hi:[0,0,0]
	v_mfma_scale_f32_16x16x128_f8f6f4 v[106:109], v[10:17], v[206:213], 0, v234, v238 op_sel_hi:[0,0,0]
	v_mfma_scale_f32_16x16x128_f8f6f4 v[102:105], v[2:9], v[216:223], 0, v234, v238 op_sel_hi:[0,0,0]
	v_mfma_scale_f32_16x16x128_f8f6f4 v[98:101], v[10:17], v[216:223], 0, v234, v238 op_sel_hi:[0,0,0]
	s_setprio 0
	s_barrier
	v_lshl_add_u64 v[172:173], s[44:45], 0, v[0:1]
	s_mov_b64 s[48:49], 0x100
	s_mov_b32 m0, s41
	v_lshl_add_u64 v[174:175], v[172:173], 0, s[48:49]
	ds_read_b128 v[198:201], v196 offset:16384
	ds_read_b128 v[202:205], v196 offset:17408
	ds_read_b128 v[206:209], v196 offset:18432
	ds_read_b128 v[210:213], v196 offset:19456
	ds_read_b128 v[216:219], v196 offset:20480
	ds_read_b128 v[220:223], v196 offset:21504
	ds_read_b128 v[224:227], v196 offset:22528
	ds_read_b128 v[228:231], v196 offset:23552
	global_load_lds_dwordx4 v[174:175], off
	v_lshl_add_u64 v[174:175], s[44:45], 0, v[166:167]
	s_add_u32 s46, s44, 0x20100
	v_lshl_add_u64 v[176:177], v[174:175], 0, s[48:49]
	s_mov_b32 m0, s57
	s_addc_u32 s47, s45, 0
	global_load_lds_dwordx4 v[176:177], off
	v_lshl_add_u64 v[176:177], s[46:47], 0, v[0:1]
	s_mov_b32 m0, s58
	s_nop 0
	global_load_lds_dwordx4 v[176:177], off
	v_lshl_add_u64 v[176:177], s[46:47], 0, v[166:167]
	s_mov_b32 m0, s59
	s_nop 0
	global_load_lds_dwordx4 v[176:177], off
	v_lshl_add_u64 v[176:177], s[42:43], 0, v[162:163]
	v_lshl_add_u64 v[178:179], v[176:177], 0, s[48:49]
	s_mov_b32 m0, s37
	s_nop 0
	global_load_lds_dwordx4 v[178:179], off
	v_lshl_add_u64 v[178:179], s[42:43], 0, v[164:165]
	v_lshl_add_u64 v[232:233], v[178:179], 0, s[48:49]
	s_mov_b32 m0, s60
	s_nop 0
	global_load_lds_dwordx4 v[232:233], off
	s_cmp_eq_u32 s26, 0
	s_cbranch_scc1 .Lrw_first_g2_1
	s_waitcnt vmcnt(24)
	s_branch .Lrw_done_g2_1

.Lrw_done_g2_1:
	s_waitcnt lgkmcnt(0)
	s_barrier
	s_setprio 1
	s_waitcnt lgkmcnt(0)
	v_mfma_scale_f32_16x16x128_f8f6f4 v[94:97], v[18:25], v[198:205], 0, v234, v238 op_sel_hi:[0,0,0]
	v_mfma_scale_f32_16x16x128_f8f6f4 v[90:93], v[26:33], v[198:205], 0, v234, v238 op_sel_hi:[0,0,0]
	v_mfma_scale_f32_16x16x128_f8f6f4 v[86:89], v[18:25], v[206:213], 0, v234, v238 op_sel_hi:[0,0,0]
	v_mfma_scale_f32_16x16x128_f8f6f4 v[82:85], v[26:33], v[206:213], 0, v234, v238 op_sel_hi:[0,0,0]
	s_setprio 0
	s_setprio 1
	v_mfma_scale_f32_16x16x128_f8f6f4 v[78:81], v[18:25], v[216:223], 0, v234, v238 op_sel_hi:[0,0,0]
	v_mfma_scale_f32_16x16x128_f8f6f4 v[74:77], v[26:33], v[216:223], 0, v234, v238 op_sel_hi:[0,0,0]
	v_mfma_scale_f32_16x16x128_f8f6f4 v[70:73], v[18:25], v[224:231], 0, v234, v238 op_sel_hi:[0,0,0]
	v_mfma_scale_f32_16x16x128_f8f6f4 v[66:69], v[26:33], v[224:231], 0, v234, v238 op_sel_hi:[0,0,0]
	s_setprio 0
	s_setprio 1
	v_mfma_scale_f32_16x16x128_f8f6f4 v[62:65], v[2:9], v[198:205], 0, v234, v238 op_sel_hi:[0,0,0]
	v_mfma_scale_f32_16x16x128_f8f6f4 v[58:61], v[10:17], v[198:205], 0, v234, v238 op_sel_hi:[0,0,0]
	v_mfma_scale_f32_16x16x128_f8f6f4 v[54:57], v[2:9], v[206:213], 0, v234, v238 op_sel_hi:[0,0,0]
	v_mfma_scale_f32_16x16x128_f8f6f4 v[50:53], v[10:17], v[206:213], 0, v234, v238 op_sel_hi:[0,0,0]
	s_setprio 0
	s_setprio 1
	v_mfma_scale_f32_16x16x128_f8f6f4 v[46:49], v[2:9], v[216:223], 0, v234, v238 op_sel_hi:[0,0,0]
	v_mfma_scale_f32_16x16x128_f8f6f4 v[42:45], v[10:17], v[216:223], 0, v234, v238 op_sel_hi:[0,0,0]
	v_mfma_scale_f32_16x16x128_f8f6f4 v[38:41], v[2:9], v[224:231], 0, v234, v238 op_sel_hi:[0,0,0]
	v_mfma_scale_f32_16x16x128_f8f6f4 v[34:37], v[10:17], v[224:231], 0, v234, v238 op_sel_hi:[0,0,0]
	s_setprio 0
	s_barrier
	ds_read_b128 v[18:21], v188
	ds_read_b128 v[22:25], v189
	ds_read_b128 v[26:29], v190
	ds_read_b128 v[30:33], v191
	ds_read_b128 v[2:5], v192
	ds_read_b128 v[6:9], v193
	ds_read_b128 v[10:13], v194
	ds_read_b128 v[14:17], v195
	s_add_u32 s46, s42, 0x20100
	s_addc_u32 s47, s43, 0
	s_mov_b32 m0, s61
	v_lshl_add_u64 v[232:233], s[46:47], 0, v[162:163]
	ds_read_b128 v[198:201], v196 offset:32768
	ds_read_b128 v[202:205], v196 offset:33792
	ds_read_b128 v[206:209], v196 offset:34816
	ds_read_b128 v[210:213], v196 offset:35840
	ds_read_b128 v[216:219], v196 offset:36864
	ds_read_b128 v[220:223], v196 offset:37888
	ds_read_b128 v[224:227], v196 offset:38912
	ds_read_b128 v[228:231], v196 offset:39936
	global_load_lds_dwordx4 v[232:233], off
	v_lshl_add_u64 v[232:233], s[46:47], 0, v[164:165]
	s_mov_b32 m0, s62
	s_nop 0
	global_load_lds_dwordx4 v[232:233], off
	s_waitcnt vmcnt(8)
	s_waitcnt lgkmcnt(0)
	s_barrier
	s_setprio 1
	s_waitcnt lgkmcnt(0)
	v_mfma_scale_f32_16x16x128_f8f6f4 v[158:161], v[18:25], v[198:205], v[158:161], v234, v238 op_sel_hi:[0,0,0]
	v_mfma_scale_f32_16x16x128_f8f6f4 v[154:157], v[26:33], v[198:205], v[154:157], v234, v238 op_sel_hi:[0,0,0]
	v_mfma_scale_f32_16x16x128_f8f6f4 v[150:153], v[18:25], v[206:213], v[150:153], v234, v238 op_sel_hi:[0,0,0]
	v_mfma_scale_f32_16x16x128_f8f6f4 v[146:149], v[26:33], v[206:213], v[146:149], v234, v238 op_sel_hi:[0,0,0]
	s_setprio 0
	s_setprio 1
	v_mfma_scale_f32_16x16x128_f8f6f4 v[142:145], v[18:25], v[216:223], v[142:145], v234, v238 op_sel_hi:[0,0,0]
	v_mfma_scale_f32_16x16x128_f8f6f4 v[138:141], v[26:33], v[216:223], v[138:141], v234, v238 op_sel_hi:[0,0,0]
	v_mfma_scale_f32_16x16x128_f8f6f4 v[134:137], v[18:25], v[224:231], v[134:137], v234, v238 op_sel_hi:[0,0,0]
	v_mfma_scale_f32_16x16x128_f8f6f4 v[130:133], v[26:33], v[224:231], v[130:133], v234, v238 op_sel_hi:[0,0,0]
	s_setprio 0
	s_setprio 1
	v_mfma_scale_f32_16x16x128_f8f6f4 v[126:129], v[2:9], v[198:205], v[126:129], v234, v238 op_sel_hi:[0,0,0]
	v_mfma_scale_f32_16x16x128_f8f6f4 v[122:125], v[10:17], v[198:205], v[122:125], v234, v238 op_sel_hi:[0,0,0]
	v_mfma_scale_f32_16x16x128_f8f6f4 v[118:121], v[2:9], v[206:213], v[118:121], v234, v238 op_sel_hi:[0,0,0]
	v_mfma_scale_f32_16x16x128_f8f6f4 v[114:117], v[10:17], v[206:213], v[114:117], v234, v238 op_sel_hi:[0,0,0]
	s_setprio 0
	s_setprio 1
	v_mfma_scale_f32_16x16x128_f8f6f4 v[110:113], v[2:9], v[216:223], v[110:113], v234, v238 op_sel_hi:[0,0,0]
	v_mfma_scale_f32_16x16x128_f8f6f4 v[106:109], v[10:17], v[216:223], v[106:109], v234, v238 op_sel_hi:[0,0,0]
	v_mfma_scale_f32_16x16x128_f8f6f4 v[102:105], v[2:9], v[224:231], v[102:105], v234, v238 op_sel_hi:[0,0,0]
	v_mfma_scale_f32_16x16x128_f8f6f4 v[98:101], v[10:17], v[224:231], v[98:101], v234, v238 op_sel_hi:[0,0,0]
	s_setprio 0
	s_barrier
	s_mov_b64 s[48:49], 0x180
	s_mov_b32 m0, s65
	v_lshl_add_u64 v[172:173], v[172:173], 0, s[48:49]
	s_add_u32 s46, s44, 0x20180
	ds_read_b128 v[198:201], v196 offset:49152
	ds_read_b128 v[202:205], v196 offset:50176
	ds_read_b128 v[206:209], v196 offset:51200
	ds_read_b128 v[210:213], v196 offset:52224
	ds_read_b128 v[216:219], v196 offset:53248
	ds_read_b128 v[220:223], v196 offset:54272
	ds_read_b128 v[224:227], v196 offset:55296
	ds_read_b128 v[228:231], v196 offset:56320
	global_load_lds_dwordx4 v[172:173], off
	v_lshl_add_u64 v[172:173], v[174:175], 0, s[48:49]
	s_mov_b32 m0, s68
	s_addc_u32 s47, s45, 0
	global_load_lds_dwordx4 v[172:173], off
	v_lshl_add_u64 v[172:173], s[46:47], 0, v[0:1]
	s_mov_b32 m0, s51
	s_nop 0
	global_load_lds_dwordx4 v[172:173], off
	v_lshl_add_u64 v[172:173], s[46:47], 0, v[166:167]
	s_mov_b32 m0, s4
	s_nop 0
	global_load_lds_dwordx4 v[172:173], off
	v_lshl_add_u64 v[172:173], v[176:177], 0, s[48:49]
	s_mov_b32 m0, s81
	s_nop 0
	global_load_lds_dwordx4 v[172:173], off
	v_lshl_add_u64 v[172:173], v[178:179], 0, s[48:49]
	s_mov_b32 m0, s50
	s_nop 0
	global_load_lds_dwordx4 v[172:173], off
	s_waitcnt vmcnt(8)
	s_waitcnt lgkmcnt(0)
	s_barrier
	s_setprio 1
	s_waitcnt lgkmcnt(0)
	v_mfma_scale_f32_16x16x128_f8f6f4 v[94:97], v[18:25], v[198:205], v[94:97], v234, v238 op_sel_hi:[0,0,0]
	v_mfma_scale_f32_16x16x128_f8f6f4 v[90:93], v[26:33], v[198:205], v[90:93], v234, v238 op_sel_hi:[0,0,0]
	v_mfma_scale_f32_16x16x128_f8f6f4 v[86:89], v[18:25], v[206:213], v[86:89], v234, v238 op_sel_hi:[0,0,0]
	v_mfma_scale_f32_16x16x128_f8f6f4 v[82:85], v[26:33], v[206:213], v[82:85], v234, v238 op_sel_hi:[0,0,0]
	s_setprio 0
	s_setprio 1
	v_mfma_scale_f32_16x16x128_f8f6f4 v[78:81], v[18:25], v[216:223], v[78:81], v234, v238 op_sel_hi:[0,0,0]
	v_mfma_scale_f32_16x16x128_f8f6f4 v[74:77], v[26:33], v[216:223], v[74:77], v234, v238 op_sel_hi:[0,0,0]
	v_mfma_scale_f32_16x16x128_f8f6f4 v[70:73], v[18:25], v[224:231], v[70:73], v234, v238 op_sel_hi:[0,0,0]
	v_mfma_scale_f32_16x16x128_f8f6f4 v[66:69], v[26:33], v[224:231], v[66:69], v234, v238 op_sel_hi:[0,0,0]
	s_setprio 0
	s_setprio 1
	v_mfma_scale_f32_16x16x128_f8f6f4 v[62:65], v[2:9], v[198:205], v[62:65], v234, v238 op_sel_hi:[0,0,0]
	v_mfma_scale_f32_16x16x128_f8f6f4 v[58:61], v[10:17], v[198:205], v[58:61], v234, v238 op_sel_hi:[0,0,0]
	v_mfma_scale_f32_16x16x128_f8f6f4 v[54:57], v[2:9], v[206:213], v[54:57], v234, v238 op_sel_hi:[0,0,0]
	v_mfma_scale_f32_16x16x128_f8f6f4 v[50:53], v[10:17], v[206:213], v[50:53], v234, v238 op_sel_hi:[0,0,0]
	s_setprio 0
	s_setprio 1
	v_mfma_scale_f32_16x16x128_f8f6f4 v[46:49], v[2:9], v[216:223], v[46:49], v234, v238 op_sel_hi:[0,0,0]
	v_mfma_scale_f32_16x16x128_f8f6f4 v[42:45], v[10:17], v[216:223], v[42:45], v234, v238 op_sel_hi:[0,0,0]
	v_mfma_scale_f32_16x16x128_f8f6f4 v[38:41], v[2:9], v[224:231], v[38:41], v234, v238 op_sel_hi:[0,0,0]
	v_mfma_scale_f32_16x16x128_f8f6f4 v[34:37], v[10:17], v[224:231], v[34:37], v234, v238 op_sel_hi:[0,0,0]
	s_setprio 0
	s_barrier
	s_add_u32 s42, s42, 0x20180
	s_addc_u32 s43, s43, 0
	s_add_u32 s48, s44, 0x200
	s_addc_u32 s49, s45, 0
	s_mov_b32 s74, 0
.LBB0_2089:
	ds_read_b128 v[2:5], v180
	ds_read_b128 v[6:9], v181
	ds_read_b128 v[10:13], v182
	ds_read_b128 v[14:17], v183
	ds_read_b128 v[26:29], v184
	ds_read_b128 v[30:33], v185
	ds_read_b128 v[172:175], v186
	ds_read_b128 v[176:179], v187
	s_add_u32 s44, s42, 0xfffe0080
	s_addc_u32 s45, s43, -1
	s_cmp_eq_u32 s74, 4
	s_cselect_b32 s47, s13, s45
	s_cselect_b32 s46, s27, s44
	s_cselect_b32 s45, s35, s49
	s_cselect_b32 s44, s34, s48
	s_mov_b32 m0, s29
	v_lshl_add_u64 v[224:225], s[42:43], 0, v[168:169]
	ds_read_b128 v[18:21], v196
	ds_read_b128 v[22:25], v196 offset:1024
	ds_read_b128 v[198:201], v196 offset:2048
	ds_read_b128 v[202:205], v196 offset:3072
	ds_read_b128 v[206:209], v196 offset:4096
	ds_read_b128 v[210:213], v196 offset:5120
	ds_read_b128 v[216:219], v196 offset:6144
	ds_read_b128 v[220:223], v196 offset:7168
	global_load_lds_dwordx4 v[224:225], off
	v_lshl_add_u64 v[224:225], s[42:43], 0, v[170:171]
	s_mov_b32 m0, s31
	s_nop 0
	global_load_lds_dwordx4 v[224:225], off
	s_waitcnt vmcnt(8)
	s_waitcnt lgkmcnt(0)
	s_barrier
	s_setprio 1
	s_waitcnt lgkmcnt(0)
	v_mfma_scale_f32_16x16x128_f8f6f4 v[158:161], v[2:9], v[18:25], v[158:161], v234, v238 op_sel_hi:[0,0,0]
	v_mfma_scale_f32_16x16x128_f8f6f4 v[154:157], v[10:17], v[18:25], v[154:157], v234, v238 op_sel_hi:[0,0,0]
	v_mfma_scale_f32_16x16x128_f8f6f4 v[150:153], v[2:9], v[198:205], v[150:153], v234, v238 op_sel_hi:[0,0,0]
	v_mfma_scale_f32_16x16x128_f8f6f4 v[146:149], v[10:17], v[198:205], v[146:149], v234, v238 op_sel_hi:[0,0,0]
	s_setprio 0
	s_setprio 1
	v_mfma_scale_f32_16x16x128_f8f6f4 v[142:145], v[2:9], v[206:213], v[142:145], v234, v238 op_sel_hi:[0,0,0]
	v_mfma_scale_f32_16x16x128_f8f6f4 v[138:141], v[10:17], v[206:213], v[138:141], v234, v238 op_sel_hi:[0,0,0]
	v_mfma_scale_f32_16x16x128_f8f6f4 v[134:137], v[2:9], v[216:223], v[134:137], v234, v238 op_sel_hi:[0,0,0]
	v_mfma_scale_f32_16x16x128_f8f6f4 v[130:133], v[10:17], v[216:223], v[130:133], v234, v238 op_sel_hi:[0,0,0]
	s_setprio 0
	s_setprio 1
	v_mfma_scale_f32_16x16x128_f8f6f4 v[126:129], v[26:33], v[18:25], v[126:129], v234, v238 op_sel_hi:[0,0,0]
	v_mfma_scale_f32_16x16x128_f8f6f4 v[122:125], v[172:179], v[18:25], v[122:125], v234, v238 op_sel_hi:[0,0,0]
	v_mfma_scale_f32_16x16x128_f8f6f4 v[118:121], v[26:33], v[198:205], v[118:121], v234, v238 op_sel_hi:[0,0,0]
	v_mfma_scale_f32_16x16x128_f8f6f4 v[114:117], v[172:179], v[198:205], v[114:117], v234, v238 op_sel_hi:[0,0,0]
	s_setprio 0
	s_setprio 1
	v_mfma_scale_f32_16x16x128_f8f6f4 v[110:113], v[26:33], v[206:213], v[110:113], v234, v238 op_sel_hi:[0,0,0]
	v_mfma_scale_f32_16x16x128_f8f6f4 v[106:109], v[172:179], v[206:213], v[106:109], v234, v238 op_sel_hi:[0,0,0]
	v_mfma_scale_f32_16x16x128_f8f6f4 v[102:105], v[26:33], v[216:223], v[102:105], v234, v238 op_sel_hi:[0,0,0]
	v_mfma_scale_f32_16x16x128_f8f6f4 v[98:101], v[172:179], v[216:223], v[98:101], v234, v238 op_sel_hi:[0,0,0]
	s_setprio 0
	s_barrier
	s_mov_b32 m0, s41
	v_lshl_add_u64 v[18:19], s[44:45], 0, v[0:1]
	s_add_u32 vcc_lo, s44, 0x20000
	ds_read_b128 v[198:201], v196 offset:16384
	ds_read_b128 v[202:205], v196 offset:17408
	ds_read_b128 v[206:209], v196 offset:18432
	ds_read_b128 v[210:213], v196 offset:19456
	ds_read_b128 v[216:219], v196 offset:20480
	ds_read_b128 v[220:223], v196 offset:21504
	ds_read_b128 v[224:227], v196 offset:22528
	ds_read_b128 v[228:231], v196 offset:23552
	global_load_lds_dwordx4 v[18:19], off
	v_lshl_add_u64 v[20:21], s[44:45], 0, v[166:167]
	s_mov_b32 m0, s57
	s_addc_u32 vcc_hi, s45, 0
	global_load_lds_dwordx4 v[20:21], off
	v_lshl_add_u64 v[22:23], vcc, 0, v[0:1]
	s_mov_b32 m0, s58
	v_lshl_add_u64 v[24:25], s[46:47], 0, v[164:165]
	global_load_lds_dwordx4 v[22:23], off
	v_lshl_add_u64 v[22:23], vcc, 0, v[166:167]
	s_mov_b32 m0, s59
	s_nop 0
	global_load_lds_dwordx4 v[22:23], off
	v_lshl_add_u64 v[22:23], s[46:47], 0, v[162:163]
	s_mov_b32 m0, s37
	s_nop 0
	global_load_lds_dwordx4 v[22:23], off
	s_mov_b32 m0, s60
	s_nop 0
	global_load_lds_dwordx4 v[24:25], off
	s_waitcnt vmcnt(8)
	s_waitcnt lgkmcnt(0)
	s_barrier
	s_setprio 1
	s_waitcnt lgkmcnt(0)
	v_mfma_scale_f32_16x16x128_f8f6f4 v[94:97], v[2:9], v[198:205], v[94:97], v234, v238 op_sel_hi:[0,0,0]
	v_mfma_scale_f32_16x16x128_f8f6f4 v[90:93], v[10:17], v[198:205], v[90:93], v234, v238 op_sel_hi:[0,0,0]
	v_mfma_scale_f32_16x16x128_f8f6f4 v[86:89], v[2:9], v[206:213], v[86:89], v234, v238 op_sel_hi:[0,0,0]
	v_mfma_scale_f32_16x16x128_f8f6f4 v[82:85], v[10:17], v[206:213], v[82:85], v234, v238 op_sel_hi:[0,0,0]
	s_setprio 0
	s_setprio 1
	v_mfma_scale_f32_16x16x128_f8f6f4 v[78:81], v[2:9], v[216:223], v[78:81], v234, v238 op_sel_hi:[0,0,0]
	v_mfma_scale_f32_16x16x128_f8f6f4 v[74:77], v[10:17], v[216:223], v[74:77], v234, v238 op_sel_hi:[0,0,0]
	v_mfma_scale_f32_16x16x128_f8f6f4 v[70:73], v[2:9], v[224:231], v[70:73], v234, v238 op_sel_hi:[0,0,0]
	v_mfma_scale_f32_16x16x128_f8f6f4 v[66:69], v[10:17], v[224:231], v[66:69], v234, v238 op_sel_hi:[0,0,0]
	s_setprio 0
	s_setprio 1
	v_mfma_scale_f32_16x16x128_f8f6f4 v[62:65], v[26:33], v[198:205], v[62:65], v234, v238 op_sel_hi:[0,0,0]
	v_mfma_scale_f32_16x16x128_f8f6f4 v[58:61], v[172:179], v[198:205], v[58:61], v234, v238 op_sel_hi:[0,0,0]
	v_mfma_scale_f32_16x16x128_f8f6f4 v[54:57], v[26:33], v[206:213], v[54:57], v234, v238 op_sel_hi:[0,0,0]
	v_mfma_scale_f32_16x16x128_f8f6f4 v[50:53], v[172:179], v[206:213], v[50:53], v234, v238 op_sel_hi:[0,0,0]
	s_setprio 0
	s_setprio 1
	v_mfma_scale_f32_16x16x128_f8f6f4 v[46:49], v[26:33], v[216:223], v[46:49], v234, v238 op_sel_hi:[0,0,0]
	v_mfma_scale_f32_16x16x128_f8f6f4 v[42:45], v[172:179], v[216:223], v[42:45], v234, v238 op_sel_hi:[0,0,0]
	v_mfma_scale_f32_16x16x128_f8f6f4 v[38:41], v[26:33], v[224:231], v[38:41], v234, v238 op_sel_hi:[0,0,0]
	v_mfma_scale_f32_16x16x128_f8f6f4 v[34:37], v[172:179], v[224:231], v[34:37], v234, v238 op_sel_hi:[0,0,0]
	s_setprio 0
	s_barrier
	ds_read_b128 v[10:13], v188
	ds_read_b128 v[14:17], v189
	ds_read_b128 v[26:29], v190
	ds_read_b128 v[30:33], v191
	ds_read_b128 v[2:5], v192
	ds_read_b128 v[6:9], v193
	ds_read_b128 v[172:175], v194
	ds_read_b128 v[176:179], v195
	s_add_u32 s46, s46, 0x20000
	s_addc_u32 s47, s47, 0
	s_mov_b32 m0, s61
	v_lshl_add_u64 v[232:233], s[46:47], 0, v[162:163]
	ds_read_b128 v[198:201], v196 offset:32768
	ds_read_b128 v[202:205], v196 offset:33792
	ds_read_b128 v[206:209], v196 offset:34816
	ds_read_b128 v[210:213], v196 offset:35840
	ds_read_b128 v[216:219], v196 offset:36864
	ds_read_b128 v[220:223], v196 offset:37888
	ds_read_b128 v[224:227], v196 offset:38912
	ds_read_b128 v[228:231], v196 offset:39936
	global_load_lds_dwordx4 v[232:233], off
	v_lshl_add_u64 v[232:233], s[46:47], 0, v[164:165]
	s_mov_b32 m0, s62
	s_nop 0
	global_load_lds_dwordx4 v[232:233], off
	s_waitcnt vmcnt(8)
	s_waitcnt lgkmcnt(0)
	s_barrier
	s_setprio 1
	s_waitcnt lgkmcnt(0)
	v_mfma_scale_f32_16x16x128_f8f6f4 v[158:161], v[10:17], v[198:205], v[158:161], v234, v238 op_sel_hi:[0,0,0]
	v_mfma_scale_f32_16x16x128_f8f6f4 v[154:157], v[26:33], v[198:205], v[154:157], v234, v238 op_sel_hi:[0,0,0]
	v_mfma_scale_f32_16x16x128_f8f6f4 v[150:153], v[10:17], v[206:213], v[150:153], v234, v238 op_sel_hi:[0,0,0]
	v_mfma_scale_f32_16x16x128_f8f6f4 v[146:149], v[26:33], v[206:213], v[146:149], v234, v238 op_sel_hi:[0,0,0]
	s_setprio 0
	s_setprio 1
	v_mfma_scale_f32_16x16x128_f8f6f4 v[142:145], v[10:17], v[216:223], v[142:145], v234, v238 op_sel_hi:[0,0,0]
	v_mfma_scale_f32_16x16x128_f8f6f4 v[138:141], v[26:33], v[216:223], v[138:141], v234, v238 op_sel_hi:[0,0,0]
	v_mfma_scale_f32_16x16x128_f8f6f4 v[134:137], v[10:17], v[224:231], v[134:137], v234, v238 op_sel_hi:[0,0,0]
	v_mfma_scale_f32_16x16x128_f8f6f4 v[130:133], v[26:33], v[224:231], v[130:133], v234, v238 op_sel_hi:[0,0,0]
	s_setprio 0
	s_setprio 1
	v_mfma_scale_f32_16x16x128_f8f6f4 v[126:129], v[2:9], v[198:205], v[126:129], v234, v238 op_sel_hi:[0,0,0]
	v_mfma_scale_f32_16x16x128_f8f6f4 v[122:125], v[172:179], v[198:205], v[122:125], v234, v238 op_sel_hi:[0,0,0]
	v_mfma_scale_f32_16x16x128_f8f6f4 v[118:121], v[2:9], v[206:213], v[118:121], v234, v238 op_sel_hi:[0,0,0]
	v_mfma_scale_f32_16x16x128_f8f6f4 v[114:117], v[172:179], v[206:213], v[114:117], v234, v238 op_sel_hi:[0,0,0]
	s_setprio 0
	s_setprio 1
	v_mfma_scale_f32_16x16x128_f8f6f4 v[110:113], v[2:9], v[216:223], v[110:113], v234, v238 op_sel_hi:[0,0,0]
	v_mfma_scale_f32_16x16x128_f8f6f4 v[106:109], v[172:179], v[216:223], v[106:109], v234, v238 op_sel_hi:[0,0,0]
	v_mfma_scale_f32_16x16x128_f8f6f4 v[102:105], v[2:9], v[224:231], v[102:105], v234, v238 op_sel_hi:[0,0,0]
	v_mfma_scale_f32_16x16x128_f8f6f4 v[98:101], v[172:179], v[224:231], v[98:101], v234, v238 op_sel_hi:[0,0,0]
	s_setprio 0
	s_barrier
	s_mov_b32 m0, s65
	v_lshl_add_u64 v[18:19], v[18:19], 0, s[66:67]
	s_add_u32 s44, s44, 0x20080
	ds_read_b128 v[198:201], v196 offset:49152
	ds_read_b128 v[202:205], v196 offset:50176
	ds_read_b128 v[206:209], v196 offset:51200
	ds_read_b128 v[210:213], v196 offset:52224
	ds_read_b128 v[216:219], v196 offset:53248
	ds_read_b128 v[220:223], v196 offset:54272
	ds_read_b128 v[224:227], v196 offset:55296
	ds_read_b128 v[228:231], v196 offset:56320
	global_load_lds_dwordx4 v[18:19], off
	v_lshl_add_u64 v[18:19], v[20:21], 0, s[66:67]
	s_mov_b32 m0, s68
	s_addc_u32 s45, s45, 0
	global_load_lds_dwordx4 v[18:19], off
	v_lshl_add_u64 v[18:19], s[44:45], 0, v[0:1]
	s_mov_b32 m0, s51
	s_nop 0
	global_load_lds_dwordx4 v[18:19], off
	v_lshl_add_u64 v[18:19], s[44:45], 0, v[166:167]
	s_mov_b32 m0, s4
	s_nop 0
	global_load_lds_dwordx4 v[18:19], off
	v_lshl_add_u64 v[18:19], v[22:23], 0, s[66:67]
	s_mov_b32 m0, s81
	s_nop 0
	global_load_lds_dwordx4 v[18:19], off
	v_lshl_add_u64 v[18:19], v[24:25], 0, s[66:67]
	s_mov_b32 m0, s50
	s_nop 0
	global_load_lds_dwordx4 v[18:19], off
	s_waitcnt vmcnt(8)
	s_waitcnt lgkmcnt(0)
	s_barrier
	s_setprio 1
	s_waitcnt lgkmcnt(0)
	v_mfma_scale_f32_16x16x128_f8f6f4 v[94:97], v[10:17], v[198:205], v[94:97], v234, v238 op_sel_hi:[0,0,0]
	v_mfma_scale_f32_16x16x128_f8f6f4 v[90:93], v[26:33], v[198:205], v[90:93], v234, v238 op_sel_hi:[0,0,0]
	v_mfma_scale_f32_16x16x128_f8f6f4 v[86:89], v[10:17], v[206:213], v[86:89], v234, v238 op_sel_hi:[0,0,0]
	v_mfma_scale_f32_16x16x128_f8f6f4 v[82:85], v[26:33], v[206:213], v[82:85], v234, v238 op_sel_hi:[0,0,0]
	s_setprio 0
	s_setprio 1
	v_mfma_scale_f32_16x16x128_f8f6f4 v[78:81], v[10:17], v[216:223], v[78:81], v234, v238 op_sel_hi:[0,0,0]
	v_mfma_scale_f32_16x16x128_f8f6f4 v[74:77], v[26:33], v[216:223], v[74:77], v234, v238 op_sel_hi:[0,0,0]
	v_mfma_scale_f32_16x16x128_f8f6f4 v[70:73], v[10:17], v[224:231], v[70:73], v234, v238 op_sel_hi:[0,0,0]
	v_mfma_scale_f32_16x16x128_f8f6f4 v[66:69], v[26:33], v[224:231], v[66:69], v234, v238 op_sel_hi:[0,0,0]
	s_setprio 0
	s_setprio 1
	v_mfma_scale_f32_16x16x128_f8f6f4 v[62:65], v[2:9], v[198:205], v[62:65], v234, v238 op_sel_hi:[0,0,0]
	v_mfma_scale_f32_16x16x128_f8f6f4 v[58:61], v[172:179], v[198:205], v[58:61], v234, v238 op_sel_hi:[0,0,0]
	v_mfma_scale_f32_16x16x128_f8f6f4 v[54:57], v[2:9], v[206:213], v[54:57], v234, v238 op_sel_hi:[0,0,0]
	v_mfma_scale_f32_16x16x128_f8f6f4 v[50:53], v[172:179], v[206:213], v[50:53], v234, v238 op_sel_hi:[0,0,0]
	s_setprio 0
	s_setprio 1
	v_mfma_scale_f32_16x16x128_f8f6f4 v[46:49], v[2:9], v[216:223], v[46:49], v234, v238 op_sel_hi:[0,0,0]
	v_mfma_scale_f32_16x16x128_f8f6f4 v[42:45], v[172:179], v[216:223], v[42:45], v234, v238 op_sel_hi:[0,0,0]
	v_mfma_scale_f32_16x16x128_f8f6f4 v[38:41], v[2:9], v[224:231], v[38:41], v234, v238 op_sel_hi:[0,0,0]
	v_mfma_scale_f32_16x16x128_f8f6f4 v[34:37], v[172:179], v[224:231], v[34:37], v234, v238 op_sel_hi:[0,0,0]
	s_setprio 0
	s_barrier
	s_add_i32 s74, s74, 2
	s_add_u32 s42, s42, 0x100
	s_addc_u32 s43, s43, 0
	s_add_u32 s48, s48, 0x100
	s_addc_u32 s49, s49, 0
	s_cmp_gt_u32 s74, 5
	s_cbranch_scc0 .LBB0_2089
	s_and_b64 vcc, exec, s[8:9]
	s_cbranch_vccz .LBB0_2092
	s_barrier
